# speedup vs baseline: 1.0030x; 1.0030x over previous
.LBB12_5:
	v_lshlrev_b32_e32 v0, 2, v0
	v_and_b32_e32 v58, 0xfc, v0
	v_lshlrev_b64 v[4:5], 11, v[4:5]
	v_lshlrev_b32_e32 v0, 2, v58
	v_mov_b32_e32 v1, 0
	s_waitcnt lgkmcnt(0)
	v_lshl_add_u64 v[4:5], s[24:25], 0, v[4:5]
	v_lshl_add_u64 v[4:5], v[4:5], 0, v[0:1]
	global_load_dwordx4 v[8:11], v[4:5], off
	global_load_dwordx4 v[12:15], v0, s[20:21]
	global_load_dwordx4 v[16:19], v0, s[20:21] offset:1024
	global_load_dwordx4 v[20:23], v[4:5], off offset:1024
	v_lshlrev_b64 v[4:5], 11, v[2:3]
	v_lshl_add_u64 v[24:25], s[22:23], 0, v[4:5]
	v_lshl_add_u64 v[40:41], v[24:25], 0, v[0:1]
	global_load_dwordx4 v[24:27], v[40:41], off
	global_load_dwordx4 v[28:31], v[40:41], off offset:1024
	global_load_dwordx4 v[32:35], v0, s[12:13]
	global_load_dwordx4 v[36:39], v0, s[12:13] offset:1024
	v_lshlrev_b64 v[6:7], 11, v[6:7]
	v_lshl_add_u64 v[6:7], s[18:19], 0, v[6:7]
	v_lshl_add_u64 v[52:53], v[6:7], 0, v[0:1]
	global_load_dwordx4 v[40:43], v0, s[14:15]
	global_load_dwordx4 v[44:47], v0, s[8:9]
	global_load_dwordx4 v[48:51], v0, s[10:11]
	v_mov_b32_e32 v59, 0x3727c5ac
	s_mov_b32 s12, 0xf800000
	v_mov_b32_e32 v60, 0x260
	v_lshl_add_u64 v[4:5], s[4:5], 0, v[4:5]
	v_lshlrev_b64 v[2:3], 10, v[2:3]
	s_waitcnt vmcnt(9)
	v_pk_add_f32 v[54:55], v[12:13], v[8:9]
	global_load_dwordx4 v[6:9], v0, s[14:15] offset:1024
	s_waitcnt vmcnt(8)
	v_pk_add_f32 v[20:21], v[16:17], v[20:21]
	v_pk_add_f32 v[18:19], v[18:19], v[22:23]
	v_pk_add_f32 v[56:57], v[14:15], v[10:11]
	global_load_dwordx4 v[10:13], v0, s[8:9] offset:1024
	global_load_dwordx4 v[14:17], v0, s[10:11] offset:1024
	s_waitcnt vmcnt(9)
	v_pk_add_f32 v[54:55], v[24:25], v[54:55]
	s_waitcnt vmcnt(8)
	v_pk_add_f32 v[28:29], v[28:29], v[20:21]
	v_pk_add_f32 v[30:31], v[30:31], v[18:19]
	global_load_dwordx4 v[18:21], v[52:53], off
	global_load_dwordx4 v[22:25], v[52:53], off offset:1024
	v_add_f32_e32 v52, 0, v54
	v_pk_add_f32 v[26:27], v[26:27], v[56:57]
	v_add_f32_e32 v52, v52, v55
	v_add_f32_e32 v52, v52, v26
	v_add_f32_e32 v52, v52, v27
	v_add_f32_e32 v52, v52, v28
	v_add_f32_e32 v52, v52, v29
	v_add_f32_e32 v52, v52, v30
	v_add_f32_e32 v52, v52, v31
	s_nop 1
	v_add_f32_dpp v52, v52, v52 quad_perm:[1,0,3,2] row_mask:0xf bank_mask:0xf bound_ctrl:1
	s_nop 1
	v_add_f32_dpp v52, v52, v52 quad_perm:[2,3,0,1] row_mask:0xf bank_mask:0xf bound_ctrl:1
	s_nop 1
	v_add_f32_dpp v52, v52, v52 row_half_mirror row_mask:0xf bank_mask:0xf bound_ctrl:1
	s_nop 1
	v_add_f32_dpp v52, v52, v52 row_mirror row_mask:0xf bank_mask:0xf bound_ctrl:1
	s_nop 0
	v_readlane_b32 s8, v52, 16
	v_readlane_b32 s9, v52, 48
	v_readlane_b32 s0, v52, 0
	v_readlane_b32 s1, v52, 32
	v_mov_b32_e32 v52, s8
	v_mov_b32_e32 v53, s9
	v_pk_add_f32 v[52:53], s[0:1], v[52:53]
	s_nop 0
	v_add_f32_e32 v52, v52, v53
	v_mul_f32_e32 v52, 0x3b000000, v52
	v_pk_add_f32 v[54:55], v[54:55], v[52:53] op_sel_hi:[1,0] neg_lo:[0,1] neg_hi:[0,1]
	v_pk_add_f32 v[26:27], v[26:27], v[52:53] op_sel_hi:[1,0] neg_lo:[0,1] neg_hi:[0,1]
	v_pk_add_f32 v[28:29], v[28:29], v[52:53] op_sel_hi:[1,0] neg_lo:[0,1] neg_hi:[0,1]
	v_pk_add_f32 v[30:31], v[30:31], v[52:53] op_sel_hi:[1,0] neg_lo:[0,1] neg_hi:[0,1]
	v_pk_mul_f32 v[52:53], v[54:55], v[54:55]
	s_waitcnt vmcnt(9)
	v_pk_mul_f32 v[32:33], v[32:33], v[54:55]
	v_add_f32_e32 v56, v52, v53
	v_pk_mul_f32 v[52:53], v[26:27], v[26:27]
	v_pk_mul_f32 v[26:27], v[34:35], v[26:27]
	v_add_f32_e32 v52, v56, v52
	v_add_f32_e32 v56, v52, v53
	v_pk_mul_f32 v[52:53], v[28:29], v[28:29]
	s_waitcnt vmcnt(8)
	v_pk_mul_f32 v[28:29], v[36:37], v[28:29]
	v_add_f32_e32 v52, v56, v52
	v_add_f32_e32 v56, v52, v53
	v_pk_mul_f32 v[52:53], v[30:31], v[30:31]
	v_pk_mul_f32 v[30:31], v[38:39], v[30:31]
	v_add_f32_e32 v52, v56, v52
	v_add_f32_e32 v52, v52, v53
	s_nop 1
	v_add_f32_dpp v52, v52, v52 quad_perm:[1,0,3,2] row_mask:0xf bank_mask:0xf bound_ctrl:1
	s_nop 1
	v_add_f32_dpp v52, v52, v52 quad_perm:[2,3,0,1] row_mask:0xf bank_mask:0xf bound_ctrl:1
	s_nop 1
	v_add_f32_dpp v52, v52, v52 row_half_mirror row_mask:0xf bank_mask:0xf bound_ctrl:1
	s_nop 1
	v_add_f32_dpp v52, v52, v52 row_mirror row_mask:0xf bank_mask:0xf bound_ctrl:1
	s_nop 0
	v_readlane_b32 s8, v52, 16
	v_readlane_b32 s9, v52, 48
	v_readlane_b32 s0, v52, 0
	v_readlane_b32 s1, v52, 32
	v_mov_b32_e32 v52, s8
	v_mov_b32_e32 v53, s9
	v_pk_add_f32 v[52:53], s[0:1], v[52:53]
	s_nop 0
	v_add_f32_e32 v52, v52, v53
	v_fmamk_f32 v52, v52, 0x3b000000, v59
	v_mul_f32_e32 v53, 0x4f800000, v52
	v_cmp_gt_f32_e32 vcc, s12, v52
	s_nop 1
	v_cndmask_b32_e32 v52, v52, v53, vcc
	v_sqrt_f32_e32 v53, v52
	s_nop 0
	v_add_u32_e32 v34, -1, v53
	v_add_u32_e32 v35, 1, v53
	v_fma_f32 v36, -v34, v53, v52
	v_fma_f32 v37, -v35, v53, v52
	v_cmp_ge_f32_e64 s[0:1], 0, v36
	s_nop 1
	v_cndmask_b32_e64 v34, v53, v34, s[0:1]
	v_cmp_lt_f32_e64 s[0:1], 0, v37
	s_nop 1
	v_cndmask_b32_e64 v34, v34, v35, s[0:1]
	v_mul_f32_e32 v35, 0x37800000, v34
	v_cndmask_b32_e32 v34, v34, v35, vcc
	v_cmp_class_f32_e32 vcc, v52, v60
	s_nop 1
	v_cndmask_b32_e32 v34, v34, v52, vcc
	v_div_scale_f32 v35, s[0:1], v34, v34, 1.0
	v_rcp_f32_e32 v36, v35
	v_div_scale_f32 v37, vcc, 1.0, v34, 1.0
	v_fma_f32 v38, -v35, v36, 1.0
	v_fmac_f32_e32 v36, v38, v36
	v_mul_f32_e32 v38, v37, v36
	v_fma_f32 v39, -v35, v38, v37
	v_fmac_f32_e32 v38, v39, v36
	v_fma_f32 v35, -v35, v38, v37
	v_div_fmas_f32 v35, v35, v36, v38
	v_div_fixup_f32 v34, v35, v34, 1.0
	s_waitcnt vmcnt(7)
	v_pk_fma_f32 v[32:33], v[34:35], v[32:33], v[40:41] op_sel_hi:[0,1,1]
	s_waitcnt vmcnt(4)
	v_pk_fma_f32 v[6:7], v[34:35], v[28:29], v[6:7] op_sel_hi:[0,1,1]
	s_waitcnt vmcnt(1)
	v_pk_add_f32 v[18:19], v[32:33], v[18:19]
	v_pk_fma_f32 v[26:27], v[34:35], v[26:27], v[42:43] op_sel_hi:[0,1,1]
	s_waitcnt vmcnt(0)
	v_pk_add_f32 v[6:7], v[6:7], v[22:23]
	v_add_f32_e32 v22, 0, v18
	v_pk_add_f32 v[20:21], v[26:27], v[20:21]
	v_add_f32_e32 v22, v22, v19
	v_add_f32_e32 v22, v22, v20
	v_add_f32_e32 v22, v22, v21
	v_pk_fma_f32 v[8:9], v[34:35], v[30:31], v[8:9] op_sel_hi:[0,1,1]
	v_add_f32_e32 v22, v22, v6
	v_pk_add_f32 v[8:9], v[8:9], v[24:25]
	v_add_f32_e32 v22, v22, v7
	v_add_f32_e32 v22, v22, v8
	v_add_f32_e32 v22, v22, v9
	s_nop 1
	v_add_f32_dpp v22, v22, v22 quad_perm:[1,0,3,2] row_mask:0xf bank_mask:0xf bound_ctrl:1
	s_nop 1
	v_add_f32_dpp v22, v22, v22 quad_perm:[2,3,0,1] row_mask:0xf bank_mask:0xf bound_ctrl:1
	s_nop 1
	v_add_f32_dpp v22, v22, v22 row_half_mirror row_mask:0xf bank_mask:0xf bound_ctrl:1
	s_nop 1
	v_add_f32_dpp v22, v22, v22 row_mirror row_mask:0xf bank_mask:0xf bound_ctrl:1
	s_nop 0
	v_readlane_b32 s8, v22, 16
	v_readlane_b32 s9, v22, 48
	v_readlane_b32 s0, v22, 0
	v_readlane_b32 s1, v22, 32
	v_mov_b32_e32 v22, s8
	v_mov_b32_e32 v23, s9
	v_pk_add_f32 v[22:23], s[0:1], v[22:23]
	s_nop 0
	v_add_f32_e32 v22, v22, v23
	v_mul_f32_e32 v22, 0x3b000000, v22
	v_pk_add_f32 v[18:19], v[18:19], v[22:23] op_sel_hi:[1,0] neg_lo:[0,1] neg_hi:[0,1]
	v_pk_add_f32 v[20:21], v[20:21], v[22:23] op_sel_hi:[1,0] neg_lo:[0,1] neg_hi:[0,1]
	v_pk_add_f32 v[24:25], v[6:7], v[22:23] op_sel_hi:[1,0] neg_lo:[0,1] neg_hi:[0,1]
	v_pk_mul_f32 v[6:7], v[18:19], v[18:19]
	v_pk_add_f32 v[22:23], v[8:9], v[22:23] op_sel_hi:[1,0] neg_lo:[0,1] neg_hi:[0,1]
	v_pk_mul_f32 v[8:9], v[20:21], v[20:21]
	v_add_f32_e32 v6, v6, v7
	v_add_f32_e32 v6, v6, v8
	v_pk_mul_f32 v[26:27], v[24:25], v[24:25]
	v_add_f32_e32 v6, v6, v9
	v_add_f32_e32 v6, v6, v26
	v_pk_mul_f32 v[28:29], v[22:23], v[22:23]
	v_add_f32_e32 v6, v6, v27
	v_add_f32_e32 v6, v6, v28
	v_add_f32_e32 v6, v6, v29
	s_nop 1
	v_add_f32_dpp v6, v6, v6 quad_perm:[1,0,3,2] row_mask:0xf bank_mask:0xf bound_ctrl:1
	s_nop 1
	v_add_f32_dpp v6, v6, v6 quad_perm:[2,3,0,1] row_mask:0xf bank_mask:0xf bound_ctrl:1
	s_nop 1
	v_add_f32_dpp v6, v6, v6 row_half_mirror row_mask:0xf bank_mask:0xf bound_ctrl:1
	s_nop 1
	v_add_f32_dpp v6, v6, v6 row_mirror row_mask:0xf bank_mask:0xf bound_ctrl:1
	s_nop 0
	v_readlane_b32 s8, v6, 16
	v_readlane_b32 s9, v6, 48
	v_readlane_b32 s0, v6, 0
	v_readlane_b32 s1, v6, 32
	v_mov_b32_e32 v6, s8
	v_mov_b32_e32 v7, s9
	v_pk_add_f32 v[6:7], s[0:1], v[6:7]
	s_nop 0
	v_add_f32_e32 v6, v6, v7
	v_fmac_f32_e32 v59, 0x3b000000, v6
	v_mul_f32_e32 v6, 0x4f800000, v59
	v_cmp_gt_f32_e32 vcc, s12, v59
	s_nop 1
	v_cndmask_b32_e32 v6, v59, v6, vcc
	v_sqrt_f32_e32 v7, v6
	s_nop 0
	v_add_u32_e32 v8, -1, v7
	v_add_u32_e32 v9, 1, v7
	v_fma_f32 v26, -v8, v7, v6
	v_fma_f32 v27, -v9, v7, v6
	v_cmp_ge_f32_e64 s[0:1], 0, v26
	s_nop 1
	v_cndmask_b32_e64 v7, v7, v8, s[0:1]
	v_cmp_lt_f32_e64 s[0:1], 0, v27
	v_lshl_add_u64 v[26:27], v[4:5], 0, v[0:1]
	s_nop 0
	v_cndmask_b32_e64 v7, v7, v9, s[0:1]
	v_mul_f32_e32 v8, 0x37800000, v7
	v_cndmask_b32_e32 v7, v7, v8, vcc
	v_cmp_class_f32_e32 vcc, v6, v60
	s_nop 1
	v_cndmask_b32_e32 v6, v7, v6, vcc
	v_div_scale_f32 v7, s[0:1], v6, v6, 1.0
	v_rcp_f32_e32 v8, v7
	s_mov_b32 s0, 0x43000000
	v_fma_f32 v0, -v7, v8, 1.0
	v_fmac_f32_e32 v8, v0, v8
	v_div_scale_f32 v0, vcc, 1.0, v6, 1.0
	v_mul_f32_e32 v4, v0, v8
	v_fma_f32 v5, -v7, v4, v0
	v_fmac_f32_e32 v4, v5, v8
	v_fma_f32 v0, -v7, v4, v0
	v_div_fmas_f32 v0, v0, v8, v4
	v_div_fixup_f32 v0, v0, v6, 1.0
	v_pk_mul_f32 v[4:5], v[44:45], v[18:19]
	v_pk_mul_f32 v[6:7], v[46:47], v[20:21]
	v_pk_fma_f32 v[4:5], v[0:1], v[4:5], v[48:49] op_sel_hi:[0,1,1]
	v_pk_mul_f32 v[8:9], v[10:11], v[24:25]
	v_pk_fma_f32 v[6:7], v[0:1], v[6:7], v[50:51] op_sel_hi:[0,1,1]
	v_pk_fma_f32 v[8:9], v[0:1], v[8:9], v[14:15] op_sel_hi:[0,1,1]
	v_pk_mul_f32 v[10:11], v[12:13], v[22:23]
	v_fma_mixlo_f16 v12, v4, s0, 0
	v_pk_fma_f32 v[10:11], v[0:1], v[10:11], v[16:17] op_sel_hi:[0,1,1]
	global_store_dwordx4 v[26:27], v[4:7], off
	global_store_dwordx4 v[26:27], v[8:11], off offset:1024
	v_mul_f32_e32 v0, 0x43000000, v4
	v_fma_mixlo_f16 v4, v4, s0, -v12 op_sel_hi:[0,0,1]
	v_fma_mixlo_f16 v12, v8, s0, 0
	v_mul_f32_e32 v13, 0x43000000, v8
	v_fma_mixlo_f16 v8, v8, s0, -v12 op_sel_hi:[0,0,1]
	v_mul_f32_e32 v12, 0x43000000, v5
	v_fma_mixlo_f16 v14, v5, s0, 0
	v_cvt_pk_f16_f32 v12, v0, v12
	v_mul_f32_e32 v0, 0x43000000, v9
	v_pk_mul_f32 v[16:17], v[6:7], s[0:1] op_sel_hi:[1,0]
	v_fma_mixhi_f16 v4, v5, s0, -v14 op_sel_hi:[0,0,1]
	v_cvt_pk_f16_f32 v14, v13, v0
	v_cvt_pk_f16_f32 v13, v16, v17
	v_pk_mul_f32 v[18:19], v[10:11], s[0:1] op_sel_hi:[1,0]
	v_cvt_f32_f16_e32 v16, v13
	v_cvt_f32_f16_sdwa v17, v13 dst_sel:DWORD dst_unused:UNUSED_PAD src0_sel:WORD_1
	v_cvt_pk_f16_f32 v15, v18, v19
	v_cvt_f32_f16_e32 v18, v15
	v_cvt_f32_f16_sdwa v19, v15 dst_sel:DWORD dst_unused:UNUSED_PAD src0_sel:WORD_1
	v_fma_mixlo_f16 v5, v9, s0, 0
	v_pk_fma_f32 v[6:7], v[6:7], s[0:1], v[16:17] op_sel_hi:[1,0,1] neg_lo:[0,0,1] neg_hi:[0,0,1]
	v_fma_mixhi_f16 v8, v9, s0, -v5 op_sel_hi:[0,0,1]
	v_cvt_pk_f16_f32 v5, v6, v7
	v_pk_fma_f32 v[6:7], v[10:11], s[0:1], v[18:19] op_sel_hi:[1,0,1] neg_lo:[0,0,1] neg_hi:[0,0,1]
	v_lshlrev_b32_e32 v0, 1, v58
	v_cvt_pk_f16_f32 v9, v6, v7
	v_lshl_add_u64 v[6:7], s[6:7], 0, v[2:3]
	v_lshl_add_u64 v[2:3], s[2:3], 0, v[2:3]
	v_lshl_add_u64 v[6:7], v[6:7], 0, v[0:1]
	v_lshl_add_u64 v[0:1], v[2:3], 0, v[0:1]
	global_store_dwordx2 v[6:7], v[12:13], off
	global_store_dwordx2 v[6:7], v[14:15], off offset:512
	global_store_dwordx2 v[0:1], v[4:5], off
	global_store_dwordx2 v[0:1], v[8:9], off offset:512
	s_endpgm
	s_endpgm
	s_endpgm
	s_endpgm
	s_endpgm
	s_endpgm
	s_endpgm
	s_endpgm
	s_endpgm
	s_endpgm
	s_endpgm
	s_endpgm
	s_endpgm
	s_endpgm
	s_endpgm
	s_endpgm
	s_endpgm
	s_endpgm
	s_endpgm
	s_endpgm
	s_endpgm
	s_endpgm
	s_endpgm
	s_endpgm
	s_endpgm
	s_endpgm
	s_endpgm
	s_endpgm
	s_endpgm
	s_endpgm
	s_endpgm
	s_endpgm
	s_endpgm
	s_endpgm
	s_endpgm
	s_endpgm
	s_endpgm
	s_endpgm
	s_endpgm
	s_endpgm
	s_endpgm
	s_endpgm
	s_endpgm
	s_endpgm
	s_endpgm
	s_endpgm

.LBB13_5:
	v_lshlrev_b32_e32 v0, 2, v0
	v_and_b32_e32 v58, 0xfc, v0
	v_lshlrev_b64 v[4:5], 11, v[4:5]
	s_load_dwordx2 s[0:1], s[0:1], 0x8
	v_lshlrev_b32_e32 v0, 2, v58
	v_mov_b32_e32 v1, 0
	s_waitcnt lgkmcnt(0)
	v_lshl_add_u64 v[4:5], s[24:25], 0, v[4:5]
	v_lshl_add_u64 v[4:5], v[4:5], 0, v[0:1]
	global_load_dwordx4 v[8:11], v[4:5], off
	global_load_dwordx4 v[12:15], v0, s[20:21]
	global_load_dwordx4 v[16:19], v0, s[20:21] offset:1024
	global_load_dwordx4 v[20:23], v[4:5], off offset:1024
	v_lshlrev_b64 v[4:5], 11, v[2:3]
	v_lshl_add_u64 v[32:33], s[22:23], 0, v[4:5]
	v_lshl_add_u64 v[34:35], v[32:33], 0, v[0:1]
	v_lshl_add_u64 v[32:33], s[0:1], 2, v[32:33]
	global_load_dwordx4 v[24:27], v[34:35], off
	global_load_dwordx4 v[28:31], v[34:35], off offset:1024
	v_lshl_add_u64 v[40:41], v[32:33], 0, v[0:1]
	global_load_dwordx4 v[32:35], v[40:41], off
	global_load_dwordx4 v[36:39], v[40:41], off offset:1024
	global_load_dwordx4 v[44:47], v0, s[12:13] offset:1024
	v_lshlrev_b64 v[6:7], 11, v[6:7]
	global_load_dwordx4 v[40:43], v0, s[12:13]
	v_lshl_add_u64 v[6:7], s[18:19], 0, v[6:7]
	global_load_dwordx4 v[48:51], v0, s[14:15]
	v_lshl_add_u64 v[52:53], v[6:7], 0, v[0:1]
	v_mov_b32_e32 v59, 0x3727c5ac
	s_mov_b32 s12, 0xf800000
	v_mov_b32_e32 v60, 0x260
	v_lshl_add_u64 v[4:5], s[4:5], 0, v[4:5]
	v_lshlrev_b64 v[2:3], 10, v[2:3]
	s_waitcnt vmcnt(9)
	v_pk_add_f32 v[54:55], v[12:13], v[8:9]
	v_pk_add_f32 v[56:57], v[14:15], v[10:11]
	s_waitcnt vmcnt(7)
	v_pk_add_f32 v[20:21], v[16:17], v[20:21]
	v_pk_add_f32 v[18:19], v[18:19], v[22:23]
	global_load_dwordx4 v[6:9], v0, s[8:9]
	global_load_dwordx4 v[10:13], v0, s[10:11]
	global_load_dwordx4 v[14:17], v0, s[14:15] offset:1024
	s_waitcnt vmcnt(9)
	v_pk_add_f32 v[54:55], v[54:55], v[24:25]
	v_pk_add_f32 v[26:27], v[56:57], v[26:27]
	s_waitcnt vmcnt(8)
	v_pk_add_f32 v[28:29], v[20:21], v[28:29]
	v_pk_add_f32 v[30:31], v[18:19], v[30:31]
	global_load_dwordx4 v[18:21], v0, s[8:9] offset:1024
	global_load_dwordx4 v[22:25], v0, s[10:11] offset:1024
	s_waitcnt vmcnt(9)
	v_pk_add_f32 v[54:55], v[54:55], v[32:33]
	v_pk_add_f32 v[34:35], v[26:27], v[34:35]
	s_waitcnt vmcnt(8)
	v_pk_add_f32 v[36:37], v[28:29], v[36:37]
	v_pk_add_f32 v[38:39], v[30:31], v[38:39]
	global_load_dwordx4 v[26:29], v[52:53], off
	global_load_dwordx4 v[30:33], v[52:53], off offset:1024
	v_add_f32_e32 v52, 0, v54
	v_add_f32_e32 v52, v52, v55
	v_add_f32_e32 v52, v52, v34
	v_add_f32_e32 v52, v52, v35
	v_add_f32_e32 v52, v52, v36
	v_add_f32_e32 v52, v52, v37
	v_add_f32_e32 v52, v52, v38
	v_add_f32_e32 v52, v52, v39
	s_nop 1
	v_add_f32_dpp v52, v52, v52 quad_perm:[1,0,3,2] row_mask:0xf bank_mask:0xf bound_ctrl:1
	s_nop 1
	v_add_f32_dpp v52, v52, v52 quad_perm:[2,3,0,1] row_mask:0xf bank_mask:0xf bound_ctrl:1
	s_nop 1
	v_add_f32_dpp v52, v52, v52 row_half_mirror row_mask:0xf bank_mask:0xf bound_ctrl:1
	s_nop 1
	v_add_f32_dpp v52, v52, v52 row_mirror row_mask:0xf bank_mask:0xf bound_ctrl:1
	s_nop 0
	v_readlane_b32 s8, v52, 16
	v_readlane_b32 s9, v52, 48
	v_readlane_b32 s0, v52, 0
	v_readlane_b32 s1, v52, 32
	v_mov_b32_e32 v52, s8
	v_mov_b32_e32 v53, s9
	v_pk_add_f32 v[52:53], s[0:1], v[52:53]
	s_nop 0
	v_add_f32_e32 v52, v52, v53
	v_mul_f32_e32 v52, 0x3b000000, v52
	v_pk_add_f32 v[54:55], v[54:55], v[52:53] op_sel_hi:[1,0] neg_lo:[0,1] neg_hi:[0,1]
	v_pk_add_f32 v[34:35], v[34:35], v[52:53] op_sel_hi:[1,0] neg_lo:[0,1] neg_hi:[0,1]
	v_pk_add_f32 v[36:37], v[36:37], v[52:53] op_sel_hi:[1,0] neg_lo:[0,1] neg_hi:[0,1]
	v_pk_add_f32 v[38:39], v[38:39], v[52:53] op_sel_hi:[1,0] neg_lo:[0,1] neg_hi:[0,1]
	v_pk_mul_f32 v[52:53], v[54:55], v[54:55]
	s_waitcnt vmcnt(8)
	v_pk_mul_f32 v[40:41], v[40:41], v[54:55]
	v_add_f32_e32 v56, v52, v53
	v_pk_mul_f32 v[52:53], v[34:35], v[34:35]
	v_pk_mul_f32 v[34:35], v[42:43], v[34:35]
	v_add_f32_e32 v52, v56, v52
	v_add_f32_e32 v56, v52, v53
	v_pk_mul_f32 v[52:53], v[36:37], v[36:37]
	v_pk_mul_f32 v[36:37], v[44:45], v[36:37]
	v_add_f32_e32 v52, v56, v52
	v_add_f32_e32 v56, v52, v53
	v_pk_mul_f32 v[52:53], v[38:39], v[38:39]
	v_pk_mul_f32 v[38:39], v[46:47], v[38:39]
	v_add_f32_e32 v52, v56, v52
	v_add_f32_e32 v52, v52, v53
	s_nop 1
	v_add_f32_dpp v52, v52, v52 quad_perm:[1,0,3,2] row_mask:0xf bank_mask:0xf bound_ctrl:1
	s_nop 1
	v_add_f32_dpp v52, v52, v52 quad_perm:[2,3,0,1] row_mask:0xf bank_mask:0xf bound_ctrl:1
	s_nop 1
	v_add_f32_dpp v52, v52, v52 row_half_mirror row_mask:0xf bank_mask:0xf bound_ctrl:1
	s_nop 1
	v_add_f32_dpp v52, v52, v52 row_mirror row_mask:0xf bank_mask:0xf bound_ctrl:1
	s_nop 0
	v_readlane_b32 s8, v52, 16
	v_readlane_b32 s9, v52, 48
	v_readlane_b32 s0, v52, 0
	v_readlane_b32 s1, v52, 32
	v_mov_b32_e32 v52, s8
	v_mov_b32_e32 v53, s9
	v_pk_add_f32 v[52:53], s[0:1], v[52:53]
	s_nop 0
	v_add_f32_e32 v52, v52, v53
	v_fmamk_f32 v52, v52, 0x3b000000, v59
	v_mul_f32_e32 v53, 0x4f800000, v52
	v_cmp_gt_f32_e32 vcc, s12, v52
	s_nop 1
	v_cndmask_b32_e32 v52, v52, v53, vcc
	v_sqrt_f32_e32 v53, v52
	s_nop 0
	v_add_u32_e32 v42, -1, v53
	v_add_u32_e32 v43, 1, v53
	v_fma_f32 v44, -v42, v53, v52
	v_fma_f32 v45, -v43, v53, v52
	v_cmp_ge_f32_e64 s[0:1], 0, v44
	s_nop 1
	v_cndmask_b32_e64 v42, v53, v42, s[0:1]
	v_cmp_lt_f32_e64 s[0:1], 0, v45
	s_nop 1
	v_cndmask_b32_e64 v42, v42, v43, s[0:1]
	v_mul_f32_e32 v43, 0x37800000, v42
	v_cndmask_b32_e32 v42, v42, v43, vcc
	v_cmp_class_f32_e32 vcc, v52, v60
	s_nop 1
	v_cndmask_b32_e32 v42, v42, v52, vcc
	v_div_scale_f32 v43, s[0:1], v42, v42, 1.0
	v_rcp_f32_e32 v44, v43
	v_div_scale_f32 v45, vcc, 1.0, v42, 1.0
	v_fma_f32 v46, -v43, v44, 1.0
	v_fmac_f32_e32 v44, v46, v44
	v_mul_f32_e32 v46, v45, v44
	v_fma_f32 v47, -v43, v46, v45
	v_fmac_f32_e32 v46, v47, v44
	v_fma_f32 v43, -v43, v46, v45
	v_div_fmas_f32 v43, v43, v44, v46
	v_div_fixup_f32 v42, v43, v42, 1.0
	s_waitcnt vmcnt(7)
	v_pk_fma_f32 v[40:41], v[42:43], v[40:41], v[48:49] op_sel_hi:[0,1,1]
	s_waitcnt vmcnt(4)
	v_pk_fma_f32 v[14:15], v[42:43], v[36:37], v[14:15] op_sel_hi:[0,1,1]
	s_waitcnt vmcnt(1)
	v_pk_add_f32 v[26:27], v[40:41], v[26:27]
	v_pk_fma_f32 v[34:35], v[42:43], v[34:35], v[50:51] op_sel_hi:[0,1,1]
	s_waitcnt vmcnt(0)
	v_pk_add_f32 v[14:15], v[14:15], v[30:31]
	v_add_f32_e32 v30, 0, v26
	v_pk_add_f32 v[28:29], v[34:35], v[28:29]
	v_add_f32_e32 v30, v30, v27
	v_add_f32_e32 v30, v30, v28
	v_add_f32_e32 v30, v30, v29
	v_pk_fma_f32 v[16:17], v[42:43], v[38:39], v[16:17] op_sel_hi:[0,1,1]
	v_add_f32_e32 v30, v30, v14
	v_pk_add_f32 v[16:17], v[16:17], v[32:33]
	v_add_f32_e32 v30, v30, v15
	v_add_f32_e32 v30, v30, v16
	v_add_f32_e32 v30, v30, v17
	s_nop 1
	v_add_f32_dpp v30, v30, v30 quad_perm:[1,0,3,2] row_mask:0xf bank_mask:0xf bound_ctrl:1
	s_nop 1
	v_add_f32_dpp v30, v30, v30 quad_perm:[2,3,0,1] row_mask:0xf bank_mask:0xf bound_ctrl:1
	s_nop 1
	v_add_f32_dpp v30, v30, v30 row_half_mirror row_mask:0xf bank_mask:0xf bound_ctrl:1
	s_nop 1
	v_add_f32_dpp v30, v30, v30 row_mirror row_mask:0xf bank_mask:0xf bound_ctrl:1
	s_nop 0
	v_readlane_b32 s8, v30, 16
	v_readlane_b32 s9, v30, 48
	v_readlane_b32 s0, v30, 0
	v_readlane_b32 s1, v30, 32
	v_mov_b32_e32 v30, s8
	v_mov_b32_e32 v31, s9
	v_pk_add_f32 v[30:31], s[0:1], v[30:31]
	s_nop 0
	v_add_f32_e32 v30, v30, v31
	v_mul_f32_e32 v30, 0x3b000000, v30
	v_pk_add_f32 v[26:27], v[26:27], v[30:31] op_sel_hi:[1,0] neg_lo:[0,1] neg_hi:[0,1]
	v_pk_add_f32 v[28:29], v[28:29], v[30:31] op_sel_hi:[1,0] neg_lo:[0,1] neg_hi:[0,1]
	v_pk_add_f32 v[14:15], v[14:15], v[30:31] op_sel_hi:[1,0] neg_lo:[0,1] neg_hi:[0,1]
	v_pk_add_f32 v[16:17], v[16:17], v[30:31] op_sel_hi:[1,0] neg_lo:[0,1] neg_hi:[0,1]
	v_pk_mul_f32 v[30:31], v[26:27], v[26:27]
	v_pk_mul_f32 v[32:33], v[28:29], v[28:29]
	v_add_f32_e32 v30, v30, v31
	v_add_f32_e32 v30, v30, v32
	v_pk_mul_f32 v[34:35], v[14:15], v[14:15]
	v_add_f32_e32 v30, v30, v33
	v_add_f32_e32 v30, v30, v34
	v_pk_mul_f32 v[36:37], v[16:17], v[16:17]
	v_add_f32_e32 v30, v30, v35
	v_add_f32_e32 v30, v30, v36
	v_add_f32_e32 v30, v30, v37
	s_nop 1
	v_add_f32_dpp v30, v30, v30 quad_perm:[1,0,3,2] row_mask:0xf bank_mask:0xf bound_ctrl:1
	s_nop 1
	v_add_f32_dpp v30, v30, v30 quad_perm:[2,3,0,1] row_mask:0xf bank_mask:0xf bound_ctrl:1
	s_nop 1
	v_add_f32_dpp v30, v30, v30 row_half_mirror row_mask:0xf bank_mask:0xf bound_ctrl:1
	s_nop 1
	v_add_f32_dpp v30, v30, v30 row_mirror row_mask:0xf bank_mask:0xf bound_ctrl:1
	s_nop 0
	v_readlane_b32 s8, v30, 16
	v_readlane_b32 s9, v30, 48
	v_readlane_b32 s0, v30, 0
	v_readlane_b32 s1, v30, 32
	v_mov_b32_e32 v30, s8
	v_mov_b32_e32 v31, s9
	v_pk_add_f32 v[30:31], s[0:1], v[30:31]
	s_nop 0
	v_add_f32_e32 v30, v30, v31
	v_fmac_f32_e32 v59, 0x3b000000, v30
	v_mul_f32_e32 v30, 0x4f800000, v59
	v_cmp_gt_f32_e32 vcc, s12, v59
	s_nop 1
	v_cndmask_b32_e32 v30, v59, v30, vcc
	v_sqrt_f32_e32 v31, v30
	s_nop 0
	v_add_u32_e32 v32, -1, v31
	v_fma_f32 v33, -v32, v31, v30
	v_cmp_ge_f32_e64 s[0:1], 0, v33
	v_add_u32_e32 v33, 1, v31
	s_nop 0
	v_cndmask_b32_e64 v32, v31, v32, s[0:1]
	v_fma_f32 v31, -v33, v31, v30
	v_cmp_lt_f32_e64 s[0:1], 0, v31
	s_nop 1
	v_cndmask_b32_e64 v31, v32, v33, s[0:1]
	v_mul_f32_e32 v32, 0x37800000, v31
	v_cndmask_b32_e32 v31, v31, v32, vcc
	v_cmp_class_f32_e32 vcc, v30, v60
	s_nop 1
	v_cndmask_b32_e32 v32, v31, v30, vcc
	v_div_scale_f32 v33, s[0:1], v32, v32, 1.0
	v_rcp_f32_e32 v34, v33
	v_lshl_add_u64 v[30:31], v[4:5], 0, v[0:1]
	s_mov_b32 s0, 0x43000000
	v_fma_f32 v0, -v33, v34, 1.0
	v_fmac_f32_e32 v34, v0, v34
	v_div_scale_f32 v0, vcc, 1.0, v32, 1.0
	v_mul_f32_e32 v4, v0, v34
	v_fma_f32 v5, -v33, v4, v0
	v_fmac_f32_e32 v4, v5, v34
	v_fma_f32 v0, -v33, v4, v0
	v_div_fmas_f32 v0, v0, v34, v4
	v_div_fixup_f32 v0, v0, v32, 1.0
	v_pk_mul_f32 v[4:5], v[6:7], v[26:27]
	v_pk_mul_f32 v[6:7], v[8:9], v[28:29]
	v_pk_fma_f32 v[4:5], v[0:1], v[4:5], v[10:11] op_sel_hi:[0,1,1]
	v_pk_mul_f32 v[8:9], v[18:19], v[14:15]
	v_pk_fma_f32 v[6:7], v[0:1], v[6:7], v[12:13] op_sel_hi:[0,1,1]
	v_pk_fma_f32 v[8:9], v[0:1], v[8:9], v[22:23] op_sel_hi:[0,1,1]
	v_pk_mul_f32 v[10:11], v[20:21], v[16:17]
	v_fma_mixlo_f16 v12, v4, s0, 0
	v_pk_fma_f32 v[10:11], v[0:1], v[10:11], v[24:25] op_sel_hi:[0,1,1]
	global_store_dwordx4 v[30:31], v[4:7], off
	global_store_dwordx4 v[30:31], v[8:11], off offset:1024
	v_mul_f32_e32 v0, 0x43000000, v4
	v_fma_mixlo_f16 v4, v4, s0, -v12 op_sel_hi:[0,0,1]
	v_fma_mixlo_f16 v12, v8, s0, 0
	v_mul_f32_e32 v13, 0x43000000, v8
	v_fma_mixlo_f16 v8, v8, s0, -v12 op_sel_hi:[0,0,1]
	v_mul_f32_e32 v12, 0x43000000, v5
	v_fma_mixlo_f16 v14, v5, s0, 0
	v_cvt_pk_f16_f32 v12, v0, v12
	v_mul_f32_e32 v0, 0x43000000, v9
	v_pk_mul_f32 v[16:17], v[6:7], s[0:1] op_sel_hi:[1,0]
	v_fma_mixhi_f16 v4, v5, s0, -v14 op_sel_hi:[0,0,1]
	v_cvt_pk_f16_f32 v14, v13, v0
	v_cvt_pk_f16_f32 v13, v16, v17
	v_pk_mul_f32 v[18:19], v[10:11], s[0:1] op_sel_hi:[1,0]
	v_cvt_f32_f16_e32 v16, v13
	v_cvt_f32_f16_sdwa v17, v13 dst_sel:DWORD dst_unused:UNUSED_PAD src0_sel:WORD_1
	v_cvt_pk_f16_f32 v15, v18, v19
	v_cvt_f32_f16_e32 v18, v15
	v_cvt_f32_f16_sdwa v19, v15 dst_sel:DWORD dst_unused:UNUSED_PAD src0_sel:WORD_1
	v_fma_mixlo_f16 v5, v9, s0, 0
	v_pk_fma_f32 v[6:7], v[6:7], s[0:1], v[16:17] op_sel_hi:[1,0,1] neg_lo:[0,0,1] neg_hi:[0,0,1]
	v_fma_mixhi_f16 v8, v9, s0, -v5 op_sel_hi:[0,0,1]
	v_cvt_pk_f16_f32 v5, v6, v7
	v_pk_fma_f32 v[6:7], v[10:11], s[0:1], v[18:19] op_sel_hi:[1,0,1] neg_lo:[0,0,1] neg_hi:[0,0,1]
	v_lshlrev_b32_e32 v0, 1, v58
	v_cvt_pk_f16_f32 v9, v6, v7
	v_lshl_add_u64 v[6:7], s[6:7], 0, v[2:3]
	v_lshl_add_u64 v[2:3], s[2:3], 0, v[2:3]
	v_lshl_add_u64 v[6:7], v[6:7], 0, v[0:1]
	v_lshl_add_u64 v[0:1], v[2:3], 0, v[0:1]
	global_store_dwordx2 v[6:7], v[12:13], off
	global_store_dwordx2 v[6:7], v[14:15], off offset:512
	global_store_dwordx2 v[0:1], v[4:5], off
	global_store_dwordx2 v[0:1], v[8:9], off offset:512
	s_endpgm
	s_endpgm
	s_endpgm
	s_endpgm
	s_endpgm
	s_endpgm
	s_endpgm
	s_endpgm
	s_endpgm
	s_endpgm
	s_endpgm
	s_endpgm
	s_endpgm
	s_endpgm
	s_endpgm
	s_endpgm
	s_endpgm
	s_endpgm
	s_endpgm
	s_endpgm
	s_endpgm
	s_endpgm
	s_endpgm
	s_endpgm
	s_endpgm
	s_endpgm
	s_endpgm

.LBB14_5:
	v_lshlrev_b32_e32 v0, 2, v0
	v_and_b32_e32 v60, 0xfc, v0
	v_lshlrev_b64 v[8:9], 11, v[8:9]
	v_lshlrev_b32_e32 v0, 2, v60
	v_mov_b32_e32 v1, 0
	s_waitcnt lgkmcnt(0)
	v_lshl_add_u64 v[8:9], s[24:25], 0, v[8:9]
	v_lshl_add_u64 v[24:25], v[8:9], 0, v[0:1]
	global_load_dwordx4 v[8:11], v[24:25], off
	global_load_dwordx4 v[12:15], v0, s[20:21]
	global_load_dwordx4 v[16:19], v0, s[20:21] offset:1024
	global_load_dwordx4 v[20:23], v[24:25], off offset:1024
	s_load_dwordx2 s[0:1], s[0:1], 0x8
	v_lshlrev_b64 v[4:5], 11, v[2:3]
	v_lshl_add_u64 v[36:37], s[22:23], 0, v[4:5]
	v_lshl_add_u64 v[28:29], v[36:37], 0, v[0:1]
	global_load_dwordx4 v[24:27], v[28:29], off
	s_waitcnt lgkmcnt(0)
	v_lshl_add_u64 v[30:31], s[0:1], 2, v[36:37]
	v_lshl_add_u64 v[38:39], v[30:31], 0, v[0:1]
	v_lshl_add_u64 v[32:33], s[0:1], 3, v[36:37]
	v_lshl_add_u64 v[44:45], v[32:33], 0, v[0:1]
	global_load_dwordx4 v[32:35], v[38:39], off
	v_mad_u64_u32 v[48:49], s[16:17], s0, 12, v[36:37]
	global_load_dwordx4 v[28:31], v[28:29], off offset:1024
	v_mov_b32_e32 v40, v49
	v_mad_u64_u32 v[46:47], s[0:1], s1, 12, v[40:41]
	global_load_dwordx4 v[40:43], v[44:45], off
	v_mov_b32_e32 v49, v46
	v_lshl_add_u64 v[56:57], v[48:49], 0, v[0:1]
	global_load_dwordx4 v[36:39], v[38:39], off offset:1024
	v_lshlrev_b64 v[6:7], 11, v[6:7]
	global_load_dwordx4 v[44:47], v[44:45], off offset:1024
	s_nop 0
	global_load_dwordx4 v[48:51], v[56:57], off
	global_load_dwordx4 v[52:55], v[56:57], off offset:1024
	v_lshl_add_u64 v[6:7], s[18:19], 0, v[6:7]
	v_lshl_add_u64 v[56:57], v[6:7], 0, v[0:1]
	v_mov_b32_e32 v61, 0x3727c5ac
	s_mov_b32 s16, 0xf800000
	v_lshl_add_u64 v[4:5], s[4:5], 0, v[4:5]
	v_lshlrev_b64 v[2:3], 10, v[2:3]
	s_waitcnt vmcnt(10)
	v_pk_add_f32 v[58:59], v[12:13], v[8:9]
	v_pk_add_f32 v[14:15], v[14:15], v[10:11]
	global_load_dwordx4 v[6:9], v0, s[12:13]
	global_load_dwordx4 v[10:13], v0, s[14:15]
	s_waitcnt vmcnt(10)
	v_pk_add_f32 v[16:17], v[16:17], v[20:21]
	v_pk_add_f32 v[18:19], v[18:19], v[22:23]
	s_waitcnt vmcnt(9)
	v_pk_add_f32 v[22:23], v[58:59], v[24:25]
	v_pk_add_f32 v[24:25], v[14:15], v[26:27]
	s_waitcnt vmcnt(8)
	v_pk_add_f32 v[32:33], v[22:23], v[32:33]
	v_pk_add_f32 v[34:35], v[24:25], v[34:35]
	s_waitcnt vmcnt(7)
	v_pk_add_f32 v[58:59], v[16:17], v[28:29]
	v_pk_add_f32 v[30:31], v[18:19], v[30:31]
	global_load_dwordx4 v[14:17], v0, s[12:13] offset:1024
	global_load_dwordx4 v[18:21], v0, s[14:15] offset:1024
	global_load_dwordx4 v[22:25], v[56:57], off
	global_load_dwordx4 v[26:29], v[56:57], off offset:1024
	s_waitcnt vmcnt(10)
	v_pk_add_f32 v[32:33], v[32:33], v[40:41]
	v_pk_add_f32 v[34:35], v[34:35], v[42:43]
	s_waitcnt vmcnt(9)
	v_pk_add_f32 v[30:31], v[30:31], v[38:39]
	v_pk_add_f32 v[36:37], v[58:59], v[36:37]
	s_waitcnt vmcnt(7)
	v_pk_add_f32 v[32:33], v[32:33], v[48:49]
	v_pk_add_f32 v[34:35], v[34:35], v[50:51]
	v_add_f32_e32 v38, 0, v32
	v_add_f32_e32 v38, v38, v33
	v_pk_add_f32 v[36:37], v[36:37], v[44:45]
	v_add_f32_e32 v38, v38, v34
	s_waitcnt vmcnt(6)
	v_pk_add_f32 v[36:37], v[36:37], v[52:53]
	v_add_f32_e32 v38, v38, v35
	v_pk_add_f32 v[30:31], v[30:31], v[46:47]
	v_add_f32_e32 v38, v38, v36
	v_pk_add_f32 v[30:31], v[30:31], v[54:55]
	v_add_f32_e32 v38, v38, v37
	v_add_f32_e32 v38, v38, v30
	v_add_f32_e32 v38, v38, v31
	v_mov_b32_e32 v55, 0x260
	s_nop 0
	v_add_f32_dpp v38, v38, v38 quad_perm:[1,0,3,2] row_mask:0xf bank_mask:0xf bound_ctrl:1
	s_nop 1
	v_add_f32_dpp v38, v38, v38 quad_perm:[2,3,0,1] row_mask:0xf bank_mask:0xf bound_ctrl:1
	s_nop 1
	v_add_f32_dpp v38, v38, v38 row_half_mirror row_mask:0xf bank_mask:0xf bound_ctrl:1
	s_nop 1
	v_add_f32_dpp v38, v38, v38 row_mirror row_mask:0xf bank_mask:0xf bound_ctrl:1
	s_nop 0
	v_readlane_b32 s12, v38, 16
	v_readlane_b32 s13, v38, 48
	v_readlane_b32 s0, v38, 0
	v_readlane_b32 s1, v38, 32
	v_mov_b32_e32 v38, s12
	v_mov_b32_e32 v39, s13
	v_pk_add_f32 v[38:39], s[0:1], v[38:39]
	s_nop 0
	v_add_f32_e32 v38, v38, v39
	v_mul_f32_e32 v38, 0x3b000000, v38
	v_pk_add_f32 v[46:47], v[32:33], v[38:39] op_sel_hi:[1,0] neg_lo:[0,1] neg_hi:[0,1]
	v_pk_add_f32 v[48:49], v[34:35], v[38:39] op_sel_hi:[1,0] neg_lo:[0,1] neg_hi:[0,1]
	v_pk_add_f32 v[52:53], v[30:31], v[38:39] op_sel_hi:[1,0] neg_lo:[0,1] neg_hi:[0,1]
	v_pk_mul_f32 v[30:31], v[46:47], v[46:47]
	v_pk_mul_f32 v[32:33], v[48:49], v[48:49]
	v_add_f32_e32 v30, v30, v31
	v_pk_add_f32 v[50:51], v[36:37], v[38:39] op_sel_hi:[1,0] neg_lo:[0,1] neg_hi:[0,1]
	v_add_f32_e32 v30, v30, v32
	v_pk_mul_f32 v[34:35], v[50:51], v[50:51]
	v_add_f32_e32 v30, v30, v33
	v_add_f32_e32 v30, v30, v34
	v_pk_mul_f32 v[36:37], v[52:53], v[52:53]
	v_add_f32_e32 v30, v30, v35
	v_add_f32_e32 v30, v30, v36
	v_add_f32_e32 v30, v30, v37
	s_waitcnt vmcnt(5)
	v_pk_mul_f32 v[6:7], v[6:7], v[46:47]
	v_add_f32_dpp v30, v30, v30 quad_perm:[1,0,3,2] row_mask:0xf bank_mask:0xf bound_ctrl:1
	v_pk_mul_f32 v[8:9], v[8:9], v[48:49]
	s_nop 0
	v_add_f32_dpp v30, v30, v30 quad_perm:[2,3,0,1] row_mask:0xf bank_mask:0xf bound_ctrl:1
	s_nop 1
	v_add_f32_dpp v30, v30, v30 row_half_mirror row_mask:0xf bank_mask:0xf bound_ctrl:1
	s_nop 1
	v_add_f32_dpp v30, v30, v30 row_mirror row_mask:0xf bank_mask:0xf bound_ctrl:1
	s_nop 0
	v_readlane_b32 s12, v30, 16
	v_readlane_b32 s13, v30, 48
	v_readlane_b32 s0, v30, 0
	v_readlane_b32 s1, v30, 32
	v_mov_b32_e32 v30, s12
	v_mov_b32_e32 v31, s13
	v_pk_add_f32 v[30:31], s[0:1], v[30:31]
	s_nop 0
	v_add_f32_e32 v30, v30, v31
	v_fmamk_f32 v30, v30, 0x3b000000, v61
	v_mul_f32_e32 v31, 0x4f800000, v30
	v_cmp_gt_f32_e32 vcc, s16, v30
	s_nop 1
	v_cndmask_b32_e32 v54, v30, v31, vcc
	v_sqrt_f32_e32 v38, v54
	global_load_dwordx4 v[30:33], v0, s[8:9]
	global_load_dwordx4 v[34:37], v0, s[10:11]
	v_add_u32_e32 v39, -1, v38
	v_add_u32_e32 v56, 1, v38
	v_fma_f32 v40, -v39, v38, v54
	v_fma_f32 v41, -v56, v38, v54
	v_cmp_ge_f32_e64 s[0:1], 0, v40
	s_nop 1
	v_cndmask_b32_e64 v57, v38, v39, s[0:1]
	v_cmp_lt_f32_e64 s[0:1], 0, v41
	global_load_dwordx4 v[38:41], v0, s[8:9] offset:1024
	global_load_dwordx4 v[42:45], v0, s[10:11] offset:1024
	v_cndmask_b32_e64 v46, v57, v56, s[0:1]
	v_mul_f32_e32 v47, 0x37800000, v46
	v_cndmask_b32_e32 v46, v46, v47, vcc
	v_cmp_class_f32_e32 vcc, v54, v55
	s_nop 1
	v_cndmask_b32_e32 v46, v46, v54, vcc
	v_div_scale_f32 v47, s[0:1], v46, v46, 1.0
	v_rcp_f32_e32 v54, v47
	v_div_scale_f32 v48, vcc, 1.0, v46, 1.0
	v_fma_f32 v49, -v47, v54, 1.0
	v_fmac_f32_e32 v54, v49, v54
	v_mul_f32_e32 v49, v48, v54
	v_fma_f32 v56, -v47, v49, v48
	v_fmac_f32_e32 v49, v56, v54
	v_fma_f32 v47, -v47, v49, v48
	v_div_fmas_f32 v47, v47, v54, v49
	v_div_fixup_f32 v46, v47, v46, 1.0
	s_waitcnt vmcnt(8)
	v_pk_fma_f32 v[6:7], v[46:47], v[6:7], v[10:11] op_sel_hi:[0,1,1]
	s_waitcnt vmcnt(5)
	v_pk_add_f32 v[6:7], v[6:7], v[22:23]
	v_pk_fma_f32 v[8:9], v[46:47], v[8:9], v[12:13] op_sel_hi:[0,1,1]
	v_pk_mul_f32 v[10:11], v[14:15], v[50:51]
	v_add_f32_e32 v14, 0, v6
	v_add_f32_e32 v14, v14, v7
	v_pk_add_f32 v[8:9], v[8:9], v[24:25]
	v_pk_fma_f32 v[10:11], v[46:47], v[10:11], v[18:19] op_sel_hi:[0,1,1]
	v_add_f32_e32 v14, v14, v8
	v_pk_mul_f32 v[12:13], v[16:17], v[52:53]
	v_add_f32_e32 v14, v14, v9
	s_waitcnt vmcnt(4)
	v_pk_add_f32 v[10:11], v[10:11], v[26:27]
	v_pk_fma_f32 v[12:13], v[46:47], v[12:13], v[20:21] op_sel_hi:[0,1,1]
	v_add_f32_e32 v14, v14, v10
	v_add_f32_e32 v14, v14, v11
	v_pk_add_f32 v[12:13], v[12:13], v[28:29]
	s_nop 0
	v_add_f32_e32 v14, v14, v12
	v_add_f32_e32 v14, v14, v13
	s_nop 1
	v_add_f32_dpp v14, v14, v14 quad_perm:[1,0,3,2] row_mask:0xf bank_mask:0xf bound_ctrl:1
	s_nop 1
	v_add_f32_dpp v14, v14, v14 quad_perm:[2,3,0,1] row_mask:0xf bank_mask:0xf bound_ctrl:1
	s_nop 1
	v_add_f32_dpp v14, v14, v14 row_half_mirror row_mask:0xf bank_mask:0xf bound_ctrl:1
	s_nop 1
	v_add_f32_dpp v14, v14, v14 row_mirror row_mask:0xf bank_mask:0xf bound_ctrl:1
	s_nop 0
	v_readlane_b32 s8, v14, 16
	v_readlane_b32 s9, v14, 48
	v_readlane_b32 s0, v14, 0
	v_readlane_b32 s1, v14, 32
	v_mov_b32_e32 v14, s8
	v_mov_b32_e32 v15, s9
	v_pk_add_f32 v[14:15], s[0:1], v[14:15]
	s_nop 0
	v_add_f32_e32 v14, v14, v15
	v_mul_f32_e32 v14, 0x3b000000, v14
	v_pk_add_f32 v[6:7], v[6:7], v[14:15] op_sel_hi:[1,0] neg_lo:[0,1] neg_hi:[0,1]
	v_pk_add_f32 v[8:9], v[8:9], v[14:15] op_sel_hi:[1,0] neg_lo:[0,1] neg_hi:[0,1]
	v_pk_mul_f32 v[16:17], v[6:7], v[6:7]
	v_pk_mul_f32 v[18:19], v[8:9], v[8:9]
	v_add_f32_e32 v16, v16, v17
	v_pk_add_f32 v[10:11], v[10:11], v[14:15] op_sel_hi:[1,0] neg_lo:[0,1] neg_hi:[0,1]
	v_add_f32_e32 v16, v16, v18
	v_pk_mul_f32 v[20:21], v[10:11], v[10:11]
	v_add_f32_e32 v16, v16, v19
	v_pk_add_f32 v[12:13], v[12:13], v[14:15] op_sel_hi:[1,0] neg_lo:[0,1] neg_hi:[0,1]
	v_add_f32_e32 v16, v16, v20
	v_pk_mul_f32 v[14:15], v[12:13], v[12:13]
	v_add_f32_e32 v16, v16, v21
	v_add_f32_e32 v14, v16, v14
	v_add_f32_e32 v14, v14, v15
	s_nop 1
	v_add_f32_dpp v14, v14, v14 quad_perm:[1,0,3,2] row_mask:0xf bank_mask:0xf bound_ctrl:1
	s_nop 1
	v_add_f32_dpp v14, v14, v14 quad_perm:[2,3,0,1] row_mask:0xf bank_mask:0xf bound_ctrl:1
	s_nop 1
	v_add_f32_dpp v14, v14, v14 row_half_mirror row_mask:0xf bank_mask:0xf bound_ctrl:1
	s_nop 1
	v_add_f32_dpp v14, v14, v14 row_mirror row_mask:0xf bank_mask:0xf bound_ctrl:1
	s_nop 0
	v_readlane_b32 s8, v14, 16
	v_readlane_b32 s9, v14, 48
	v_readlane_b32 s0, v14, 0
	v_readlane_b32 s1, v14, 32
	v_mov_b32_e32 v14, s8
	v_mov_b32_e32 v15, s9
	v_pk_add_f32 v[14:15], s[0:1], v[14:15]
	s_nop 0
	v_add_f32_e32 v14, v14, v15
	v_fmac_f32_e32 v61, 0x3b000000, v14
	v_mul_f32_e32 v14, 0x4f800000, v61
	v_cmp_gt_f32_e32 vcc, s16, v61
	s_nop 1
	v_cndmask_b32_e32 v14, v61, v14, vcc
	v_sqrt_f32_e32 v15, v14
	s_nop 0
	v_add_u32_e32 v16, -1, v15
	v_fma_f32 v17, -v16, v15, v14
	v_cmp_ge_f32_e64 s[0:1], 0, v17
	v_add_u32_e32 v17, 1, v15
	s_nop 0
	v_cndmask_b32_e64 v16, v15, v16, s[0:1]
	v_fma_f32 v15, -v17, v15, v14
	v_cmp_lt_f32_e64 s[0:1], 0, v15
	s_nop 1
	v_cndmask_b32_e64 v15, v16, v17, s[0:1]
	v_mul_f32_e32 v16, 0x37800000, v15
	v_cndmask_b32_e32 v15, v15, v16, vcc
	v_cmp_class_f32_e32 vcc, v14, v55
	s_nop 1
	v_cndmask_b32_e32 v16, v15, v14, vcc
	v_div_scale_f32 v17, s[0:1], v16, v16, 1.0
	v_rcp_f32_e32 v18, v17
	v_lshl_add_u64 v[14:15], v[4:5], 0, v[0:1]
	s_mov_b32 s0, 0x43000000
	v_fma_f32 v0, -v17, v18, 1.0
	v_fmac_f32_e32 v18, v0, v18
	v_div_scale_f32 v0, vcc, 1.0, v16, 1.0
	v_mul_f32_e32 v4, v0, v18
	v_fma_f32 v5, -v17, v4, v0
	v_fmac_f32_e32 v4, v5, v18
	v_fma_f32 v0, -v17, v4, v0
	v_div_fmas_f32 v0, v0, v18, v4
	v_div_fixup_f32 v0, v0, v16, 1.0
	s_waitcnt vmcnt(3)
	v_pk_mul_f32 v[4:5], v[30:31], v[6:7]
	v_pk_mul_f32 v[6:7], v[32:33], v[8:9]
	s_waitcnt vmcnt(2)
	v_pk_fma_f32 v[4:5], v[0:1], v[4:5], v[34:35] op_sel_hi:[0,1,1]
	s_waitcnt vmcnt(1)
	v_pk_mul_f32 v[8:9], v[38:39], v[10:11]
	v_pk_fma_f32 v[6:7], v[0:1], v[6:7], v[36:37] op_sel_hi:[0,1,1]
	s_waitcnt vmcnt(0)
	v_pk_fma_f32 v[8:9], v[0:1], v[8:9], v[42:43] op_sel_hi:[0,1,1]
	v_pk_mul_f32 v[10:11], v[40:41], v[12:13]
	v_fma_mixlo_f16 v12, v4, s0, 0
	v_pk_fma_f32 v[10:11], v[0:1], v[10:11], v[44:45] op_sel_hi:[0,1,1]
	global_store_dwordx4 v[14:15], v[4:7], off
	global_store_dwordx4 v[14:15], v[8:11], off offset:1024
	v_mul_f32_e32 v0, 0x43000000, v4
	v_fma_mixlo_f16 v4, v4, s0, -v12 op_sel_hi:[0,0,1]
	v_fma_mixlo_f16 v12, v8, s0, 0
	v_mul_f32_e32 v13, 0x43000000, v8
	v_fma_mixlo_f16 v8, v8, s0, -v12 op_sel_hi:[0,0,1]
	v_mul_f32_e32 v12, 0x43000000, v5
	v_fma_mixlo_f16 v14, v5, s0, 0
	v_cvt_pk_f16_f32 v12, v0, v12
	v_mul_f32_e32 v0, 0x43000000, v9
	v_pk_mul_f32 v[16:17], v[6:7], s[0:1] op_sel_hi:[1,0]
	v_fma_mixhi_f16 v4, v5, s0, -v14 op_sel_hi:[0,0,1]
	v_cvt_pk_f16_f32 v14, v13, v0
	v_cvt_pk_f16_f32 v13, v16, v17
	v_pk_mul_f32 v[18:19], v[10:11], s[0:1] op_sel_hi:[1,0]
	v_cvt_f32_f16_e32 v16, v13
	v_cvt_f32_f16_sdwa v17, v13 dst_sel:DWORD dst_unused:UNUSED_PAD src0_sel:WORD_1
	v_cvt_pk_f16_f32 v15, v18, v19
	v_cvt_f32_f16_e32 v18, v15
	v_cvt_f32_f16_sdwa v19, v15 dst_sel:DWORD dst_unused:UNUSED_PAD src0_sel:WORD_1
	v_fma_mixlo_f16 v5, v9, s0, 0
	v_pk_fma_f32 v[6:7], v[6:7], s[0:1], v[16:17] op_sel_hi:[1,0,1] neg_lo:[0,0,1] neg_hi:[0,0,1]
	v_fma_mixhi_f16 v8, v9, s0, -v5 op_sel_hi:[0,0,1]
	v_cvt_pk_f16_f32 v5, v6, v7
	v_pk_fma_f32 v[6:7], v[10:11], s[0:1], v[18:19] op_sel_hi:[1,0,1] neg_lo:[0,0,1] neg_hi:[0,0,1]
	v_lshlrev_b32_e32 v0, 1, v60
	v_cvt_pk_f16_f32 v9, v6, v7
	v_lshl_add_u64 v[6:7], s[6:7], 0, v[2:3]
	v_lshl_add_u64 v[2:3], s[2:3], 0, v[2:3]
	v_lshl_add_u64 v[6:7], v[6:7], 0, v[0:1]
	v_lshl_add_u64 v[0:1], v[2:3], 0, v[0:1]
	global_store_dwordx2 v[6:7], v[12:13], off
	global_store_dwordx2 v[6:7], v[14:15], off offset:512
	global_store_dwordx2 v[0:1], v[4:5], off
	global_store_dwordx2 v[0:1], v[8:9], off offset:512
	s_endpgm
	s_endpgm
	s_endpgm
	s_endpgm
	s_endpgm
	s_endpgm
	s_endpgm
	s_endpgm
	s_endpgm
	s_endpgm
	s_endpgm
	s_endpgm
	s_endpgm
	s_endpgm
	s_endpgm
	s_endpgm
	s_endpgm
	s_endpgm
	s_endpgm
	s_endpgm
	s_endpgm
	s_endpgm
	s_endpgm
	s_endpgm
	s_endpgm
	s_endpgm
	s_endpgm
	s_endpgm
	s_endpgm
	s_endpgm
	s_endpgm
	s_endpgm
	s_endpgm
	s_endpgm
	s_endpgm
	s_endpgm
	s_endpgm
	s_endpgm
	s_endpgm
	s_endpgm
	s_endpgm
	s_endpgm
	s_endpgm
	s_endpgm
	s_endpgm
	s_endpgm
	s_endpgm
	s_endpgm
	s_endpgm

.LBB15_5:
	v_lshlrev_b32_e32 v0, 2, v0
	v_and_b32_e32 v8, 0xfc, v0
	v_lshlrev_b64 v[4:5], 11, v[4:5]
	v_lshlrev_b32_e32 v0, 2, v8
	v_mov_b32_e32 v1, 0
	s_waitcnt lgkmcnt(0)
	v_lshl_add_u64 v[4:5], s[24:25], 0, v[4:5]
	v_lshl_add_u64 v[4:5], v[4:5], 0, v[0:1]
	global_load_dwordx4 v[10:13], v[4:5], off
	global_load_dwordx4 v[14:17], v0, s[20:21]
	global_load_dwordx4 v[18:21], v0, s[20:21] offset:1024
	global_load_dwordx4 v[22:25], v[4:5], off offset:1024
	s_load_dwordx2 s[0:1], s[0:1], 0x8
	v_lshlrev_b64 v[4:5], 11, v[2:3]
	v_lshl_add_u64 v[50:51], s[22:23], 0, v[4:5]
	v_lshl_add_u64 v[30:31], v[50:51], 0, v[0:1]
	global_load_dwordx4 v[26:29], v[30:31], off
	s_waitcnt lgkmcnt(0)
	v_lshl_add_u64 v[34:35], s[0:1], 2, v[50:51]
	global_load_dwordx4 v[30:33], v[30:31], off offset:1024
	v_lshl_add_u64 v[42:43], v[34:35], 0, v[0:1]
	global_load_dwordx4 v[34:37], v[42:43], off
	global_load_dwordx4 v[38:41], v[42:43], off offset:1024
	v_lshl_add_u64 v[42:43], s[0:1], 3, v[50:51]
	v_lshl_add_u64 v[52:53], v[42:43], 0, v[0:1]
	global_load_dwordx4 v[42:45], v[52:53], off
	global_load_dwordx4 v[46:49], v[52:53], off offset:1024
	v_mad_u64_u32 v[52:53], s[16:17], s0, 12, v[50:51]
	v_mad_u64_u32 v[56:57], s[16:17], s0, 20, v[50:51]
	v_mad_u64_u32 v[62:63], s[16:17], s0, 24, v[50:51]
	v_lshl_add_u64 v[54:55], s[0:1], 4, v[50:51]
	v_mad_u64_u32 v[50:51], s[16:17], s0, 28, v[50:51]
	v_lshl_add_u64 v[54:55], v[54:55], 0, v[0:1]
	v_lshlrev_b64 v[6:7], 11, v[6:7]
	v_lshl_add_u64 v[6:7], s[18:19], 0, v[6:7]
	v_lshl_add_u64 v[6:7], v[6:7], 0, v[0:1]
	v_lshl_add_u64 v[4:5], s[4:5], 0, v[4:5]
	v_lshlrev_b64 v[2:3], 10, v[2:3]
	s_waitcnt vmcnt(8)
	v_pk_add_f32 v[58:59], v[14:15], v[10:11]
	v_mov_b32_e32 v10, v53
	v_pk_add_f32 v[60:61], v[16:17], v[12:13]
	v_mov_b32_e32 v12, v57
	v_mad_u64_u32 v[10:11], s[16:17], s1, 12, v[10:11]
	v_mov_b32_e32 v53, v10
	v_mov_b32_e32 v10, v63
	v_mad_u64_u32 v[12:13], s[16:17], s1, 20, v[12:13]
	v_mov_b32_e32 v57, v12
	v_mov_b32_e32 v12, v51
	v_mad_u64_u32 v[10:11], s[16:17], s1, 24, v[10:11]
	s_waitcnt vmcnt(6)
	v_pk_add_f32 v[66:67], v[18:19], v[22:23]
	v_lshl_add_u64 v[22:23], v[52:53], 0, v[0:1]
	v_mad_u64_u32 v[64:65], s[0:1], s1, 28, v[12:13]
	v_mov_b32_e32 v63, v10
	v_pk_add_f32 v[68:69], v[20:21], v[24:25]
	global_load_dwordx4 v[10:13], v[54:55], off
	global_load_dwordx4 v[14:17], v[54:55], off offset:1024
	global_load_dwordx4 v[18:21], v[22:23], off
	v_lshl_add_u64 v[52:53], v[56:57], 0, v[0:1]
	s_waitcnt vmcnt(8)
	v_pk_add_f32 v[54:55], v[58:59], v[26:27]
	v_pk_add_f32 v[56:57], v[60:61], v[28:29]
	global_load_dwordx4 v[26:29], v[52:53], off
	v_lshl_add_u64 v[58:59], v[62:63], 0, v[0:1]
	global_load_dwordx4 v[22:25], v[22:23], off offset:1024
	v_mov_b32_e32 v51, v64
	s_waitcnt vmcnt(9)
	v_pk_add_f32 v[60:61], v[66:67], v[30:31]
	v_pk_add_f32 v[62:63], v[68:69], v[32:33]
	s_waitcnt vmcnt(8)
	v_pk_add_f32 v[54:55], v[54:55], v[34:35]
	v_pk_add_f32 v[56:57], v[56:57], v[36:37]
	global_load_dwordx4 v[30:33], v[52:53], off offset:1024
	global_load_dwordx4 v[34:37], v[58:59], off
	v_lshl_add_u64 v[50:51], v[50:51], 0, v[0:1]
	s_waitcnt vmcnt(9)
	v_pk_add_f32 v[52:53], v[60:61], v[38:39]
	v_pk_add_f32 v[60:61], v[62:63], v[40:41]
	s_waitcnt vmcnt(8)
	v_pk_add_f32 v[54:55], v[54:55], v[42:43]
	v_pk_add_f32 v[56:57], v[56:57], v[44:45]
	global_load_dwordx4 v[38:41], v[50:51], off
	global_load_dwordx4 v[42:45], v[58:59], off offset:1024
	s_waitcnt vmcnt(9)
	v_pk_add_f32 v[52:53], v[52:53], v[46:47]
	v_pk_add_f32 v[58:59], v[60:61], v[48:49]
	global_load_dwordx4 v[46:49], v[50:51], off offset:1024
	s_waitcnt vmcnt(7)
	v_pk_add_f32 v[18:19], v[54:55], v[18:19]
	s_nop 0
	v_pk_add_f32 v[10:11], v[18:19], v[10:11]
	v_pk_add_f32 v[20:21], v[56:57], v[20:21]
	v_mov_b32_e32 v57, 0x3727c5ac
	s_waitcnt vmcnt(6)
	v_pk_add_f32 v[18:19], v[10:11], v[26:27]
	v_pk_add_f32 v[12:13], v[20:21], v[12:13]
	s_waitcnt vmcnt(5)
	v_pk_add_f32 v[22:23], v[52:53], v[22:23]
	v_pk_add_f32 v[10:11], v[58:59], v[24:25]
	v_pk_add_f32 v[14:15], v[22:23], v[14:15]
	v_pk_add_f32 v[10:11], v[10:11], v[16:17]
	v_pk_add_f32 v[20:21], v[12:13], v[28:29]
	v_mov_b32_e32 v58, 0x260
	s_waitcnt vmcnt(4)
	v_pk_add_f32 v[50:51], v[14:15], v[30:31]
	v_pk_add_f32 v[52:53], v[10:11], v[32:33]
	global_load_dwordx4 v[10:13], v0, s[12:13]
	global_load_dwordx4 v[14:17], v0, s[14:15]
	s_waitcnt vmcnt(5)
	v_pk_add_f32 v[18:19], v[18:19], v[34:35]
	s_waitcnt vmcnt(4)
	v_pk_add_f32 v[34:35], v[18:19], v[38:39]
	v_pk_add_f32 v[18:19], v[20:21], v[36:37]
	v_add_f32_e32 v9, 0, v34
	v_pk_add_f32 v[36:37], v[18:19], v[40:41]
	global_load_dwordx4 v[18:21], v0, s[12:13] offset:1024
	global_load_dwordx4 v[22:25], v0, s[14:15] offset:1024
	global_load_dwordx4 v[26:29], v[6:7], off
	global_load_dwordx4 v[30:33], v[6:7], off offset:1024
	v_add_f32_e32 v9, v9, v35
	v_add_f32_e32 v9, v9, v36
	s_waitcnt vmcnt(7)
	v_pk_add_f32 v[6:7], v[50:51], v[42:43]
	v_add_f32_e32 v9, v9, v37
	s_waitcnt vmcnt(6)
	v_pk_add_f32 v[6:7], v[6:7], v[46:47]
	v_pk_add_f32 v[38:39], v[52:53], v[44:45]
	v_add_f32_e32 v9, v9, v6
	v_add_f32_e32 v9, v9, v7
	v_pk_add_f32 v[38:39], v[38:39], v[48:49]
	s_nop 0
	v_add_f32_e32 v9, v9, v38
	v_add_f32_e32 v9, v9, v39
	s_nop 1
	v_add_f32_dpp v9, v9, v9 quad_perm:[1,0,3,2] row_mask:0xf bank_mask:0xf bound_ctrl:1
	s_nop 1
	v_add_f32_dpp v9, v9, v9 quad_perm:[2,3,0,1] row_mask:0xf bank_mask:0xf bound_ctrl:1
	s_nop 1
	v_add_f32_dpp v9, v9, v9 row_half_mirror row_mask:0xf bank_mask:0xf bound_ctrl:1
	s_nop 1
	v_add_f32_dpp v9, v9, v9 row_mirror row_mask:0xf bank_mask:0xf bound_ctrl:1
	s_nop 0
	v_readlane_b32 s12, v9, 16
	v_readlane_b32 s13, v9, 48
	v_readlane_b32 s0, v9, 0
	v_readlane_b32 s1, v9, 32
	v_mov_b32_e32 v40, s12
	v_mov_b32_e32 v41, s13
	v_pk_add_f32 v[40:41], s[0:1], v[40:41]
	s_nop 0
	v_add_f32_e32 v9, v40, v41
	v_mul_f32_e32 v40, 0x3b000000, v9
	v_pk_add_f32 v[50:51], v[34:35], v[40:41] op_sel_hi:[1,0] neg_lo:[0,1] neg_hi:[0,1]
	v_pk_add_f32 v[52:53], v[36:37], v[40:41] op_sel_hi:[1,0] neg_lo:[0,1] neg_hi:[0,1]
	v_pk_mul_f32 v[34:35], v[50:51], v[50:51]
	v_pk_mul_f32 v[36:37], v[52:53], v[52:53]
	v_add_f32_e32 v9, v34, v35
	v_pk_add_f32 v[6:7], v[6:7], v[40:41] op_sel_hi:[1,0] neg_lo:[0,1] neg_hi:[0,1]
	v_add_f32_e32 v9, v9, v36
	v_pk_mul_f32 v[42:43], v[6:7], v[6:7]
	v_add_f32_e32 v9, v9, v37
	v_pk_add_f32 v[54:55], v[38:39], v[40:41] op_sel_hi:[1,0] neg_lo:[0,1] neg_hi:[0,1]
	v_add_f32_e32 v9, v9, v42
	v_pk_mul_f32 v[38:39], v[54:55], v[54:55]
	v_add_f32_e32 v9, v9, v43
	v_add_f32_e32 v9, v9, v38
	v_add_f32_e32 v9, v9, v39
	s_waitcnt vmcnt(5)
	v_pk_mul_f32 v[10:11], v[10:11], v[50:51]
	v_add_f32_dpp v9, v9, v9 quad_perm:[1,0,3,2] row_mask:0xf bank_mask:0xf bound_ctrl:1
	v_pk_mul_f32 v[12:13], v[12:13], v[52:53]
	s_waitcnt vmcnt(3)
	v_pk_mul_f32 v[6:7], v[18:19], v[6:7]
	v_add_f32_dpp v9, v9, v9 quad_perm:[2,3,0,1] row_mask:0xf bank_mask:0xf bound_ctrl:1
	s_nop 1
	v_add_f32_dpp v9, v9, v9 row_half_mirror row_mask:0xf bank_mask:0xf bound_ctrl:1
	s_nop 1
	v_add_f32_dpp v9, v9, v9 row_mirror row_mask:0xf bank_mask:0xf bound_ctrl:1
	s_nop 0
	v_readlane_b32 s12, v9, 16
	v_readlane_b32 s13, v9, 48
	v_readlane_b32 s0, v9, 0
	v_readlane_b32 s1, v9, 32
	v_mov_b32_e32 v34, s12
	v_mov_b32_e32 v35, s13
	v_pk_add_f32 v[34:35], s[0:1], v[34:35]
	s_mov_b32 s12, 0xf800000
	v_add_f32_e32 v9, v34, v35
	v_fmamk_f32 v9, v9, 0x3b000000, v57
	v_mul_f32_e32 v34, 0x4f800000, v9
	v_cmp_gt_f32_e32 vcc, s12, v9
	s_nop 1
	v_cndmask_b32_e32 v9, v9, v34, vcc
	v_sqrt_f32_e32 v34, v9
	s_nop 0
	v_add_u32_e32 v35, -1, v34
	v_fma_f32 v36, -v35, v34, v9
	v_cmp_ge_f32_e64 s[0:1], 0, v36
	v_add_u32_e32 v36, 1, v34
	s_nop 0
	v_cndmask_b32_e64 v35, v34, v35, s[0:1]
	v_fma_f32 v34, -v36, v34, v9
	v_cmp_lt_f32_e64 s[0:1], 0, v34
	s_nop 1
	v_cndmask_b32_e64 v34, v35, v36, s[0:1]
	v_mul_f32_e32 v35, 0x37800000, v34
	v_cndmask_b32_e32 v34, v34, v35, vcc
	v_cmp_class_f32_e32 vcc, v9, v58
	s_nop 1
	v_cndmask_b32_e32 v9, v34, v9, vcc
	v_div_scale_f32 v42, s[0:1], v9, v9, 1.0
	v_rcp_f32_e32 v43, v42
	global_load_dwordx4 v[34:37], v0, s[8:9]
	global_load_dwordx4 v[38:41], v0, s[10:11]
	v_fma_f32 v44, -v42, v43, 1.0
	v_fmac_f32_e32 v43, v44, v43
	v_div_scale_f32 v44, vcc, 1.0, v9, 1.0
	v_mul_f32_e32 v45, v44, v43
	v_fma_f32 v46, -v42, v45, v44
	v_fmac_f32_e32 v45, v46, v43
	v_fma_f32 v42, -v42, v45, v44
	v_div_fmas_f32 v56, v42, v43, v45
	global_load_dwordx4 v[42:45], v0, s[8:9] offset:1024
	global_load_dwordx4 v[46:49], v0, s[10:11] offset:1024
	v_div_fixup_f32 v56, v56, v9, 1.0
	v_pk_fma_f32 v[10:11], v[56:57], v[10:11], v[14:15] op_sel_hi:[0,1,1]
	s_waitcnt vmcnt(5)
	v_pk_add_f32 v[10:11], v[10:11], v[26:27]
	v_pk_fma_f32 v[12:13], v[56:57], v[12:13], v[16:17] op_sel_hi:[0,1,1]
	v_add_f32_e32 v9, 0, v10
	v_add_f32_e32 v9, v9, v11
	v_pk_add_f32 v[12:13], v[12:13], v[28:29]
	v_pk_fma_f32 v[6:7], v[56:57], v[6:7], v[22:23] op_sel_hi:[0,1,1]
	v_add_f32_e32 v9, v9, v12
	v_pk_mul_f32 v[14:15], v[20:21], v[54:55]
	v_add_f32_e32 v9, v9, v13
	s_waitcnt vmcnt(4)
	v_pk_add_f32 v[6:7], v[6:7], v[30:31]
	v_pk_fma_f32 v[14:15], v[56:57], v[14:15], v[24:25] op_sel_hi:[0,1,1]
	v_add_f32_e32 v9, v9, v6
	v_add_f32_e32 v9, v9, v7
	v_pk_add_f32 v[14:15], v[14:15], v[32:33]
	s_nop 0
	v_add_f32_e32 v9, v9, v14
	v_add_f32_e32 v9, v9, v15
	s_nop 1
	v_add_f32_dpp v9, v9, v9 quad_perm:[1,0,3,2] row_mask:0xf bank_mask:0xf bound_ctrl:1
	s_nop 1
	v_add_f32_dpp v9, v9, v9 quad_perm:[2,3,0,1] row_mask:0xf bank_mask:0xf bound_ctrl:1
	s_nop 1
	v_add_f32_dpp v9, v9, v9 row_half_mirror row_mask:0xf bank_mask:0xf bound_ctrl:1
	s_nop 1
	v_add_f32_dpp v9, v9, v9 row_mirror row_mask:0xf bank_mask:0xf bound_ctrl:1
	s_nop 0
	v_readlane_b32 s8, v9, 16
	v_readlane_b32 s9, v9, 48
	v_readlane_b32 s0, v9, 0
	v_readlane_b32 s1, v9, 32
	v_mov_b32_e32 v16, s8
	v_mov_b32_e32 v17, s9
	v_pk_add_f32 v[16:17], s[0:1], v[16:17]
	s_nop 0
	v_add_f32_e32 v9, v16, v17
	v_mul_f32_e32 v16, 0x3b000000, v9
	v_pk_add_f32 v[10:11], v[10:11], v[16:17] op_sel_hi:[1,0] neg_lo:[0,1] neg_hi:[0,1]
	v_pk_add_f32 v[12:13], v[12:13], v[16:17] op_sel_hi:[1,0] neg_lo:[0,1] neg_hi:[0,1]
	v_pk_mul_f32 v[18:19], v[10:11], v[10:11]
	v_pk_mul_f32 v[20:21], v[12:13], v[12:13]
	v_add_f32_e32 v9, v18, v19
	v_pk_add_f32 v[22:23], v[6:7], v[16:17] op_sel_hi:[1,0] neg_lo:[0,1] neg_hi:[0,1]
	v_add_f32_e32 v9, v9, v20
	v_pk_mul_f32 v[6:7], v[22:23], v[22:23]
	v_add_f32_e32 v9, v9, v21
	v_pk_add_f32 v[14:15], v[14:15], v[16:17] op_sel_hi:[1,0] neg_lo:[0,1] neg_hi:[0,1]
	v_add_f32_e32 v6, v9, v6
	v_pk_mul_f32 v[16:17], v[14:15], v[14:15]
	v_add_f32_e32 v6, v6, v7
	v_add_f32_e32 v6, v6, v16
	v_add_f32_e32 v6, v6, v17
	s_nop 1
	v_add_f32_dpp v6, v6, v6 quad_perm:[1,0,3,2] row_mask:0xf bank_mask:0xf bound_ctrl:1
	s_nop 1
	v_add_f32_dpp v6, v6, v6 quad_perm:[2,3,0,1] row_mask:0xf bank_mask:0xf bound_ctrl:1
	s_nop 1
	v_add_f32_dpp v6, v6, v6 row_half_mirror row_mask:0xf bank_mask:0xf bound_ctrl:1
	s_nop 1
	v_add_f32_dpp v6, v6, v6 row_mirror row_mask:0xf bank_mask:0xf bound_ctrl:1
	s_nop 0
	v_readlane_b32 s8, v6, 16
	v_readlane_b32 s9, v6, 48
	v_readlane_b32 s0, v6, 0
	v_readlane_b32 s1, v6, 32
	v_mov_b32_e32 v6, s8
	v_mov_b32_e32 v7, s9
	v_pk_add_f32 v[6:7], s[0:1], v[6:7]
	s_nop 0
	v_add_f32_e32 v6, v6, v7
	v_fmac_f32_e32 v57, 0x3b000000, v6
	v_mul_f32_e32 v6, 0x4f800000, v57
	v_cmp_gt_f32_e32 vcc, s12, v57
	s_nop 1
	v_cndmask_b32_e32 v6, v57, v6, vcc
	v_sqrt_f32_e32 v7, v6
	s_nop 0
	v_add_u32_e32 v9, -1, v7
	v_fma_f32 v16, -v9, v7, v6
	v_cmp_ge_f32_e64 s[0:1], 0, v16
	v_add_u32_e32 v16, 1, v7
	s_nop 0
	v_cndmask_b32_e64 v9, v7, v9, s[0:1]
	v_fma_f32 v7, -v16, v7, v6
	v_cmp_lt_f32_e64 s[0:1], 0, v7
	s_nop 1
	v_cndmask_b32_e64 v7, v9, v16, s[0:1]
	v_mul_f32_e32 v9, 0x37800000, v7
	v_cndmask_b32_e32 v7, v7, v9, vcc
	v_cmp_class_f32_e32 vcc, v6, v58
	v_lshl_add_u64 v[16:17], v[4:5], 0, v[0:1]
	s_nop 0
	v_cndmask_b32_e32 v6, v7, v6, vcc
	v_div_scale_f32 v7, s[0:1], v6, v6, 1.0
	v_rcp_f32_e32 v9, v7
	s_mov_b32 s0, 0x43000000
	v_fma_f32 v0, -v7, v9, 1.0
	v_fmac_f32_e32 v9, v0, v9
	v_div_scale_f32 v0, vcc, 1.0, v6, 1.0
	v_mul_f32_e32 v4, v0, v9
	v_fma_f32 v5, -v7, v4, v0
	v_fmac_f32_e32 v4, v5, v9
	v_fma_f32 v0, -v7, v4, v0
	v_div_fmas_f32 v0, v0, v9, v4
	v_div_fixup_f32 v0, v0, v6, 1.0
	s_waitcnt vmcnt(3)
	v_pk_mul_f32 v[4:5], v[34:35], v[10:11]
	v_pk_mul_f32 v[6:7], v[36:37], v[12:13]
	s_waitcnt vmcnt(2)
	v_pk_fma_f32 v[4:5], v[0:1], v[4:5], v[38:39] op_sel_hi:[0,1,1]
	v_pk_fma_f32 v[6:7], v[0:1], v[6:7], v[40:41] op_sel_hi:[0,1,1]
	s_waitcnt vmcnt(1)
	v_pk_mul_f32 v[10:11], v[42:43], v[22:23]
	v_pk_mul_f32 v[12:13], v[44:45], v[14:15]
	v_fma_mixlo_f16 v9, v4, s0, 0
	s_waitcnt vmcnt(0)
	v_pk_fma_f32 v[10:11], v[0:1], v[10:11], v[46:47] op_sel_hi:[0,1,1]
	v_pk_fma_f32 v[12:13], v[0:1], v[12:13], v[48:49] op_sel_hi:[0,1,1]
	global_store_dwordx4 v[16:17], v[4:7], off
	global_store_dwordx4 v[16:17], v[10:13], off offset:1024
	v_mul_f32_e32 v0, 0x43000000, v4
	v_fma_mixlo_f16 v4, v4, s0, -v9 op_sel_hi:[0,0,1]
	v_fma_mixlo_f16 v15, v5, s0, 0
	v_pk_mul_f32 v[18:19], v[6:7], s[0:1] op_sel_hi:[1,0]
	v_fma_mixhi_f16 v4, v5, s0, -v15 op_sel_hi:[0,0,1]
	v_cvt_pk_f16_f32 v15, v18, v19
	v_pk_mul_f32 v[20:21], v[12:13], s[0:1] op_sel_hi:[1,0]
	v_cvt_f32_f16_e32 v18, v15
	v_cvt_f32_f16_sdwa v19, v15 dst_sel:DWORD dst_unused:UNUSED_PAD src0_sel:WORD_1
	v_cvt_pk_f16_f32 v17, v20, v21
	v_cvt_f32_f16_e32 v20, v17
	v_cvt_f32_f16_sdwa v21, v17 dst_sel:DWORD dst_unused:UNUSED_PAD src0_sel:WORD_1
	v_fma_mixlo_f16 v14, v10, s0, 0
	v_mul_f32_e32 v9, 0x43000000, v10
	v_fma_mixlo_f16 v10, v10, s0, -v14 op_sel_hi:[0,0,1]
	v_mul_f32_e32 v14, 0x43000000, v5
	v_fma_mixlo_f16 v5, v11, s0, 0
	v_pk_fma_f32 v[6:7], v[6:7], s[0:1], v[18:19] op_sel_hi:[1,0,1] neg_lo:[0,0,1] neg_hi:[0,0,1]
	v_cvt_pk_f16_f32 v14, v0, v14
	v_mul_f32_e32 v0, 0x43000000, v11
	v_fma_mixhi_f16 v10, v11, s0, -v5 op_sel_hi:[0,0,1]
	v_cvt_pk_f16_f32 v5, v6, v7
	v_pk_fma_f32 v[6:7], v[12:13], s[0:1], v[20:21] op_sel_hi:[1,0,1] neg_lo:[0,0,1] neg_hi:[0,0,1]
	v_cvt_pk_f16_f32 v16, v9, v0
	v_cvt_pk_f16_f32 v11, v6, v7
	v_lshl_add_u64 v[6:7], s[6:7], 0, v[2:3]
	v_lshlrev_b32_e32 v0, 1, v8
	v_lshl_add_u64 v[2:3], s[2:3], 0, v[2:3]
	v_lshl_add_u64 v[6:7], v[6:7], 0, v[0:1]
	v_lshl_add_u64 v[0:1], v[2:3], 0, v[0:1]
	global_store_dwordx2 v[6:7], v[14:15], off
	global_store_dwordx2 v[6:7], v[16:17], off offset:512
	global_store_dwordx2 v[0:1], v[4:5], off
	global_store_dwordx2 v[0:1], v[10:11], off offset:512
	s_endpgm
	s_endpgm
	s_endpgm
	s_endpgm
	s_endpgm
	s_endpgm
	s_endpgm
	s_endpgm
	s_endpgm
	s_endpgm
	s_endpgm
	s_endpgm
	s_endpgm
	s_endpgm
	s_endpgm
	s_endpgm
	s_endpgm
	s_endpgm
	s_endpgm
	s_endpgm
	s_endpgm
	s_endpgm
	s_endpgm
	s_endpgm
	s_endpgm
	s_endpgm
	s_endpgm
	s_endpgm
	s_endpgm

.LBB19_5:
	v_lshlrev_b32_e32 v0, 2, v0
	v_and_b32_e32 v50, 0xfc, v0
	v_lshlrev_b64 v[2:3], 11, v[2:3]
	v_lshlrev_b32_e32 v4, 2, v50
	v_mov_b32_e32 v5, 0
	s_waitcnt lgkmcnt(0)
	v_lshl_add_u64 v[2:3], s[14:15], 0, v[2:3]
	v_lshlrev_b64 v[36:37], 11, v[6:7]
	v_lshl_add_u64 v[2:3], v[2:3], 0, v[4:5]
	v_lshl_add_u64 v[0:1], s[18:19], 0, v[36:37]
	global_load_dwordx4 v[8:11], v[2:3], off
	global_load_dwordx4 v[12:15], v4, s[16:17]
	global_load_dwordx4 v[16:19], v4, s[16:17] offset:1024
	global_load_dwordx4 v[20:23], v[2:3], off offset:1024
	v_lshl_add_u64 v[38:39], v[0:1], 0, v[4:5]
	global_load_dwordx4 v[24:27], v[38:39], off
	global_load_dwordx4 v[28:31], v[38:39], off offset:1024
	global_load_dwordx4 v[32:35], v4, s[4:5]
	global_load_dwordx4 v[0:3], v4, s[4:5] offset:1024
	v_lshl_add_u64 v[36:37], s[8:9], 0, v[36:37]
	v_lshl_add_u64 v[48:49], v[36:37], 0, v[4:5]
	global_load_dwordx4 v[36:39], v4, s[6:7]
	global_load_dwordx4 v[40:43], v4, s[6:7] offset:1024
	v_lshlrev_b64 v[6:7], 10, v[6:7]
	v_lshl_add_u64 v[44:45], s[10:11], 0, v[6:7]
	v_lshl_add_u64 v[46:47], s[2:3], 0, v[6:7]
	v_mov_b32_e32 v51, 0x3727c5ac
	s_mov_b32 s5, 0xf800000
	v_mov_b32_e32 v52, 0x260
	s_mov_b32 s4, 0x43000000
	v_lshlrev_b32_e32 v4, 1, v50
	v_lshl_add_u64 v[44:45], v[44:45], 0, v[4:5]
	s_waitcnt vmcnt(8)
	v_pk_add_f32 v[6:7], v[12:13], v[8:9]
	s_waitcnt vmcnt(5)
	v_pk_add_f32 v[6:7], v[24:25], v[6:7]
	v_pk_add_f32 v[8:9], v[14:15], v[10:11]
	v_add_f32_e32 v14, 0, v6
	v_pk_add_f32 v[8:9], v[26:27], v[8:9]
	v_add_f32_e32 v14, v14, v7
	v_pk_add_f32 v[10:11], v[16:17], v[20:21]
	v_add_f32_e32 v14, v14, v8
	s_waitcnt vmcnt(4)
	v_pk_add_f32 v[10:11], v[28:29], v[10:11]
	v_add_f32_e32 v14, v14, v9
	v_pk_add_f32 v[12:13], v[18:19], v[22:23]
	v_add_f32_e32 v14, v14, v10
	v_pk_add_f32 v[12:13], v[30:31], v[12:13]
	v_add_f32_e32 v14, v14, v11
	v_add_f32_e32 v14, v14, v12
	v_add_f32_e32 v14, v14, v13
	s_nop 1
	v_add_f32_dpp v14, v14, v14 quad_perm:[1,0,3,2] row_mask:0xf bank_mask:0xf bound_ctrl:1
	s_nop 1
	v_add_f32_dpp v14, v14, v14 quad_perm:[2,3,0,1] row_mask:0xf bank_mask:0xf bound_ctrl:1
	s_nop 1
	v_add_f32_dpp v14, v14, v14 row_half_mirror row_mask:0xf bank_mask:0xf bound_ctrl:1
	s_nop 1
	v_add_f32_dpp v14, v14, v14 row_mirror row_mask:0xf bank_mask:0xf bound_ctrl:1
	s_nop 0
	v_readlane_b32 s2, v14, 16
	v_readlane_b32 s3, v14, 48
	v_readlane_b32 s0, v14, 0
	v_readlane_b32 s1, v14, 32
	v_mov_b32_e32 v14, s2
	v_mov_b32_e32 v15, s3
	v_pk_add_f32 v[14:15], s[0:1], v[14:15]
	s_nop 0
	v_add_f32_e32 v14, v14, v15
	v_mul_f32_e32 v14, 0x3b000000, v14
	v_pk_add_f32 v[6:7], v[6:7], v[14:15] op_sel_hi:[1,0] neg_lo:[0,1] neg_hi:[0,1]
	v_pk_add_f32 v[8:9], v[8:9], v[14:15] op_sel_hi:[1,0] neg_lo:[0,1] neg_hi:[0,1]
	v_pk_add_f32 v[10:11], v[10:11], v[14:15] op_sel_hi:[1,0] neg_lo:[0,1] neg_hi:[0,1]
	v_pk_add_f32 v[12:13], v[12:13], v[14:15] op_sel_hi:[1,0] neg_lo:[0,1] neg_hi:[0,1]
	v_pk_mul_f32 v[14:15], v[6:7], v[6:7]
	v_pk_mul_f32 v[16:17], v[8:9], v[8:9]
	v_add_f32_e32 v14, v14, v15
	v_add_f32_e32 v14, v14, v16
	v_pk_mul_f32 v[18:19], v[10:11], v[10:11]
	v_add_f32_e32 v14, v14, v17
	v_add_f32_e32 v14, v14, v18
	v_pk_mul_f32 v[20:21], v[12:13], v[12:13]
	v_add_f32_e32 v14, v14, v19
	v_add_f32_e32 v14, v14, v20
	v_add_f32_e32 v14, v14, v21
	s_waitcnt vmcnt(2)
	v_pk_mul_f32 v[10:11], v[0:1], v[10:11]
	v_pk_mul_f32 v[12:13], v[2:3], v[12:13]
	v_add_f32_dpp v14, v14, v14 quad_perm:[1,0,3,2] row_mask:0xf bank_mask:0xf bound_ctrl:1
	v_pk_mul_f32 v[6:7], v[32:33], v[6:7]
	v_pk_mul_f32 v[8:9], v[34:35], v[8:9]
	v_add_f32_dpp v14, v14, v14 quad_perm:[2,3,0,1] row_mask:0xf bank_mask:0xf bound_ctrl:1
	s_nop 1
	v_add_f32_dpp v14, v14, v14 row_half_mirror row_mask:0xf bank_mask:0xf bound_ctrl:1
	s_nop 1
	v_add_f32_dpp v14, v14, v14 row_mirror row_mask:0xf bank_mask:0xf bound_ctrl:1
	s_nop 0
	v_readlane_b32 s2, v14, 16
	v_readlane_b32 s3, v14, 48
	v_readlane_b32 s0, v14, 0
	v_readlane_b32 s1, v14, 32
	v_mov_b32_e32 v14, s2
	v_mov_b32_e32 v15, s3
	v_pk_add_f32 v[14:15], s[0:1], v[14:15]
	s_nop 0
	v_add_f32_e32 v14, v14, v15
	v_fmac_f32_e32 v51, 0x3b000000, v14
	v_mul_f32_e32 v14, 0x4f800000, v51
	v_cmp_gt_f32_e32 vcc, s5, v51
	s_nop 1
	v_cndmask_b32_e32 v14, v51, v14, vcc
	v_sqrt_f32_e32 v15, v14
	s_nop 0
	v_add_u32_e32 v0, -1, v15
	v_add_u32_e32 v1, 1, v15
	v_fma_f32 v16, -v0, v15, v14
	v_fma_f32 v17, -v1, v15, v14
	v_cmp_ge_f32_e64 s[0:1], 0, v16
	s_nop 1
	v_cndmask_b32_e64 v0, v15, v0, s[0:1]
	v_cmp_lt_f32_e64 s[0:1], 0, v17
	s_nop 1
	v_cndmask_b32_e64 v0, v0, v1, s[0:1]
	v_mul_f32_e32 v1, 0x37800000, v0
	v_cndmask_b32_e32 v0, v0, v1, vcc
	v_cmp_class_f32_e32 vcc, v14, v52
	s_nop 1
	v_cndmask_b32_e32 v0, v0, v14, vcc
	v_div_scale_f32 v1, s[0:1], v0, v0, 1.0
	v_rcp_f32_e32 v14, v1
	v_div_scale_f32 v2, vcc, 1.0, v0, 1.0
	v_fma_f32 v3, -v1, v14, 1.0
	v_fmac_f32_e32 v14, v3, v14
	v_mul_f32_e32 v3, v2, v14
	v_fma_f32 v15, -v1, v3, v2
	v_fmac_f32_e32 v3, v15, v14
	v_fma_f32 v1, -v1, v3, v2
	v_div_fmas_f32 v1, v1, v14, v3
	v_div_fixup_f32 v14, v1, v0, 1.0
	s_waitcnt vmcnt(1)
	v_pk_fma_f32 v[0:1], v[14:15], v[6:7], v[36:37] op_sel_hi:[0,1,1]
	v_pk_fma_f32 v[2:3], v[14:15], v[8:9], v[38:39] op_sel_hi:[0,1,1]
	s_waitcnt vmcnt(0)
	v_pk_fma_f32 v[6:7], v[14:15], v[10:11], v[40:41] op_sel_hi:[0,1,1]
	v_pk_fma_f32 v[8:9], v[14:15], v[12:13], v[42:43] op_sel_hi:[0,1,1]
	v_fma_mixlo_f16 v15, v0, s4, 0
	v_pk_mul_f32 v[10:11], v[2:3], s[4:5] op_sel_hi:[1,0]
	global_store_dwordx4 v[48:49], v[0:3], off
	global_store_dwordx4 v[48:49], v[6:9], off offset:1024
	v_mul_f32_e32 v14, 0x43000000, v0
	v_fma_mixlo_f16 v17, v6, s4, 0
	v_pk_mul_f32 v[12:13], v[8:9], s[4:5] op_sel_hi:[1,0]
	v_fma_mixlo_f16 v0, v0, s4, -v15 op_sel_hi:[0,0,1]
	v_cvt_pk_f16_f32 v15, v10, v11
	v_mul_f32_e32 v16, 0x43000000, v6
	v_fma_mixlo_f16 v6, v6, s4, -v17 op_sel_hi:[0,0,1]
	v_cvt_pk_f16_f32 v17, v12, v13
	v_cvt_f32_f16_e32 v10, v15
	v_cvt_f32_f16_sdwa v11, v15 dst_sel:DWORD dst_unused:UNUSED_PAD src0_sel:WORD_1
	v_cvt_f32_f16_e32 v12, v17
	v_cvt_f32_f16_sdwa v13, v17 dst_sel:DWORD dst_unused:UNUSED_PAD src0_sel:WORD_1
	v_mul_f32_e32 v18, 0x43000000, v1
	v_fma_mixlo_f16 v19, v1, s4, 0
	v_pk_fma_f32 v[2:3], v[2:3], s[4:5], v[10:11] op_sel_hi:[1,0,1] neg_lo:[0,0,1] neg_hi:[0,0,1]
	v_mul_f32_e32 v20, 0x43000000, v7
	v_fma_mixlo_f16 v21, v7, s4, 0
	v_cvt_pk_f16_f32 v14, v14, v18
	v_fma_mixhi_f16 v0, v1, s4, -v19 op_sel_hi:[0,0,1]
	v_pk_fma_f32 v[8:9], v[8:9], s[4:5], v[12:13] op_sel_hi:[1,0,1] neg_lo:[0,0,1] neg_hi:[0,0,1]
	v_cvt_pk_f16_f32 v1, v2, v3
	v_lshl_add_u64 v[2:3], v[46:47], 0, v[4:5]
	v_cvt_pk_f16_f32 v16, v16, v20
	v_fma_mixhi_f16 v6, v7, s4, -v21 op_sel_hi:[0,0,1]
	global_store_dwordx2 v[44:45], v[14:15], off
	global_store_dwordx2 v[44:45], v[16:17], off offset:512
	v_cvt_pk_f16_f32 v7, v8, v9
	global_store_dwordx2 v[2:3], v[0:1], off
	global_store_dwordx2 v[2:3], v[6:7], off offset:512
	s_endpgm
	s_endpgm
	s_endpgm
	s_endpgm
	s_endpgm
	s_endpgm
	s_endpgm
	s_endpgm
	s_endpgm
	s_endpgm
	s_endpgm
	s_endpgm

.LBB20_5:
	v_lshlrev_b32_e32 v0, 2, v0
	s_load_dwordx2 s[0:1], s[0:1], 0x8
	v_and_b32_e32 v54, 0xfc, v0
	v_lshlrev_b64 v[44:45], 11, v[2:3]
	v_lshlrev_b64 v[4:5], 11, v[4:5]
	s_waitcnt lgkmcnt(0)
	v_lshl_add_u64 v[24:25], s[18:19], 0, v[44:45]
	v_lshlrev_b32_e32 v0, 2, v54
	v_mov_b32_e32 v1, 0
	v_lshl_add_u64 v[4:5], s[14:15], 0, v[4:5]
	v_lshl_add_u64 v[20:21], v[4:5], 0, v[0:1]
	v_lshl_add_u64 v[26:27], v[24:25], 0, v[0:1]
	global_load_dwordx4 v[4:7], v[20:21], off
	global_load_dwordx4 v[8:11], v0, s[16:17]
	global_load_dwordx4 v[12:15], v0, s[16:17] offset:1024
	global_load_dwordx4 v[16:19], v[20:21], off offset:1024
	v_lshl_add_u64 v[28:29], s[0:1], 2, v[24:25]
	global_load_dwordx4 v[20:23], v[26:27], off
	v_lshl_add_u64 v[46:47], v[28:29], 0, v[0:1]
	global_load_dwordx4 v[24:27], v[26:27], off offset:1024
	s_nop 0
	global_load_dwordx4 v[28:31], v[46:47], off
	global_load_dwordx4 v[32:35], v[46:47], off offset:1024
	global_load_dwordx4 v[36:39], v0, s[8:9]
	global_load_dwordx4 v[40:43], v0, s[8:9] offset:1024
	v_lshl_add_u64 v[44:45], s[4:5], 0, v[44:45]
	v_lshl_add_u64 v[52:53], v[44:45], 0, v[0:1]
	global_load_dwordx4 v[44:47], v0, s[10:11]
	global_load_dwordx4 v[48:51], v0, s[10:11] offset:1024
	v_mov_b32_e32 v55, 0x3727c5ac
	s_mov_b32 s9, 0xf800000
	v_mov_b32_e32 v56, 0x260
	s_mov_b32 s8, 0x43000000
	v_lshlrev_b64 v[2:3], 10, v[2:3]
	s_waitcnt vmcnt(10)
	v_pk_add_f32 v[4:5], v[8:9], v[4:5]
	v_pk_add_f32 v[6:7], v[10:11], v[6:7]
	s_waitcnt vmcnt(8)
	v_pk_add_f32 v[8:9], v[12:13], v[16:17]
	v_pk_add_f32 v[10:11], v[14:15], v[18:19]
	s_waitcnt vmcnt(7)
	v_pk_add_f32 v[4:5], v[4:5], v[20:21]
	v_pk_add_f32 v[6:7], v[6:7], v[22:23]
	s_waitcnt vmcnt(5)
	v_pk_add_f32 v[4:5], v[4:5], v[28:29]
	v_pk_add_f32 v[6:7], v[6:7], v[30:31]
	v_add_f32_e32 v0, 0, v4
	v_add_f32_e32 v0, v0, v5
	v_pk_add_f32 v[8:9], v[8:9], v[24:25]
	v_add_f32_e32 v0, v0, v6
	s_waitcnt vmcnt(4)
	v_pk_add_f32 v[8:9], v[8:9], v[32:33]
	v_add_f32_e32 v0, v0, v7
	v_pk_add_f32 v[10:11], v[10:11], v[26:27]
	v_add_f32_e32 v0, v0, v8
	v_pk_add_f32 v[10:11], v[10:11], v[34:35]
	v_add_f32_e32 v0, v0, v9
	v_add_f32_e32 v0, v0, v10
	v_add_f32_e32 v0, v0, v11
	s_nop 1
	v_add_f32_dpp v0, v0, v0 quad_perm:[1,0,3,2] row_mask:0xf bank_mask:0xf bound_ctrl:1
	s_nop 1
	v_add_f32_dpp v0, v0, v0 quad_perm:[2,3,0,1] row_mask:0xf bank_mask:0xf bound_ctrl:1
	s_nop 1
	v_add_f32_dpp v0, v0, v0 row_half_mirror row_mask:0xf bank_mask:0xf bound_ctrl:1
	s_nop 1
	v_add_f32_dpp v0, v0, v0 row_mirror row_mask:0xf bank_mask:0xf bound_ctrl:1
	s_nop 0
	v_readlane_b32 s4, v0, 16
	v_readlane_b32 s5, v0, 48
	v_readlane_b32 s0, v0, 0
	v_readlane_b32 s1, v0, 32
	v_mov_b32_e32 v12, s4
	v_mov_b32_e32 v13, s5
	v_pk_add_f32 v[12:13], s[0:1], v[12:13]
	s_nop 0
	v_add_f32_e32 v0, v12, v13
	v_mul_f32_e32 v0, 0x3b000000, v0
	v_pk_add_f32 v[4:5], v[4:5], v[0:1] op_sel_hi:[1,0] neg_lo:[0,1] neg_hi:[0,1]
	v_pk_add_f32 v[6:7], v[6:7], v[0:1] op_sel_hi:[1,0] neg_lo:[0,1] neg_hi:[0,1]
	v_pk_mul_f32 v[12:13], v[4:5], v[4:5]
	v_pk_add_f32 v[8:9], v[8:9], v[0:1] op_sel_hi:[1,0] neg_lo:[0,1] neg_hi:[0,1]
	v_pk_add_f32 v[10:11], v[10:11], v[0:1] op_sel_hi:[1,0] neg_lo:[0,1] neg_hi:[0,1]
	v_pk_mul_f32 v[14:15], v[6:7], v[6:7]
	v_add_f32_e32 v0, v12, v13
	v_add_f32_e32 v0, v0, v14
	v_pk_mul_f32 v[16:17], v[8:9], v[8:9]
	v_add_f32_e32 v0, v0, v15
	v_add_f32_e32 v0, v0, v16
	v_pk_mul_f32 v[18:19], v[10:11], v[10:11]
	v_add_f32_e32 v0, v0, v17
	v_add_f32_e32 v0, v0, v18
	v_add_f32_e32 v0, v0, v19
	s_waitcnt vmcnt(3)
	v_pk_mul_f32 v[6:7], v[38:39], v[6:7]
	s_waitcnt vmcnt(2)
	v_pk_mul_f32 v[8:9], v[40:41], v[8:9]
	v_add_f32_dpp v0, v0, v0 quad_perm:[1,0,3,2] row_mask:0xf bank_mask:0xf bound_ctrl:1
	v_pk_mul_f32 v[4:5], v[36:37], v[4:5]
	v_pk_mul_f32 v[10:11], v[42:43], v[10:11]
	v_add_f32_dpp v0, v0, v0 quad_perm:[2,3,0,1] row_mask:0xf bank_mask:0xf bound_ctrl:1
	s_nop 1
	v_add_f32_dpp v0, v0, v0 row_half_mirror row_mask:0xf bank_mask:0xf bound_ctrl:1
	s_nop 1
	v_add_f32_dpp v0, v0, v0 row_mirror row_mask:0xf bank_mask:0xf bound_ctrl:1
	s_nop 0
	v_readlane_b32 s4, v0, 16
	v_readlane_b32 s5, v0, 48
	v_readlane_b32 s0, v0, 0
	v_readlane_b32 s1, v0, 32
	v_mov_b32_e32 v12, s4
	v_mov_b32_e32 v13, s5
	v_pk_add_f32 v[12:13], s[0:1], v[12:13]
	s_nop 0
	v_add_f32_e32 v0, v12, v13
	v_fmac_f32_e32 v55, 0x3b000000, v0
	v_mul_f32_e32 v0, 0x4f800000, v55
	v_cmp_gt_f32_e32 vcc, s9, v55
	s_nop 1
	v_cndmask_b32_e32 v0, v55, v0, vcc
	v_sqrt_f32_e32 v12, v0
	s_nop 0
	v_add_u32_e32 v13, -1, v12
	v_add_u32_e32 v14, 1, v12
	v_fma_f32 v15, -v13, v12, v0
	v_fma_f32 v16, -v14, v12, v0
	v_cmp_ge_f32_e64 s[0:1], 0, v15
	s_nop 1
	v_cndmask_b32_e64 v12, v12, v13, s[0:1]
	v_cmp_lt_f32_e64 s[0:1], 0, v16
	s_nop 1
	v_cndmask_b32_e64 v12, v12, v14, s[0:1]
	v_mul_f32_e32 v13, 0x37800000, v12
	v_cndmask_b32_e32 v12, v12, v13, vcc
	v_cmp_class_f32_e32 vcc, v0, v56
	s_nop 1
	v_cndmask_b32_e32 v0, v12, v0, vcc
	v_div_scale_f32 v12, s[0:1], v0, v0, 1.0
	v_rcp_f32_e32 v13, v12
	v_div_scale_f32 v14, vcc, 1.0, v0, 1.0
	v_fma_f32 v15, -v12, v13, 1.0
	v_fmac_f32_e32 v13, v15, v13
	v_mul_f32_e32 v15, v14, v13
	v_fma_f32 v16, -v12, v15, v14
	v_fmac_f32_e32 v15, v16, v13
	v_fma_f32 v12, -v12, v15, v14
	v_div_fmas_f32 v12, v12, v13, v15
	v_div_fixup_f32 v0, v12, v0, 1.0
	s_waitcnt vmcnt(1)
	v_pk_fma_f32 v[6:7], v[0:1], v[6:7], v[46:47] op_sel_hi:[0,1,1]
	s_waitcnt vmcnt(0)
	v_pk_fma_f32 v[8:9], v[0:1], v[8:9], v[48:49] op_sel_hi:[0,1,1]
	v_pk_fma_f32 v[4:5], v[0:1], v[4:5], v[44:45] op_sel_hi:[0,1,1]
	v_mul_f32_e32 v17, 0x43000000, v8
	v_fma_mixlo_f16 v18, v8, s8, 0
	v_mul_f32_e32 v21, 0x43000000, v9
	v_pk_mul_f32 v[12:13], v[6:7], s[8:9] op_sel_hi:[1,0]
	v_pk_fma_f32 v[10:11], v[0:1], v[10:11], v[50:51] op_sel_hi:[0,1,1]
	global_store_dwordx4 v[52:53], v[4:7], off
	global_store_dwordx4 v[52:53], v[8:11], off offset:1024
	v_mul_f32_e32 v0, 0x43000000, v4
	v_fma_mixlo_f16 v16, v4, s8, 0
	v_fma_mixlo_f16 v8, v8, s8, -v18 op_sel_hi:[0,0,1]
	v_cvt_pk_f16_f32 v18, v17, v21
	v_cvt_pk_f16_f32 v17, v12, v13
	v_mul_f32_e32 v19, 0x43000000, v5
	v_pk_mul_f32 v[14:15], v[10:11], s[8:9] op_sel_hi:[1,0]
	v_cvt_f32_f16_e32 v12, v17
	v_cvt_f32_f16_sdwa v13, v17 dst_sel:DWORD dst_unused:UNUSED_PAD src0_sel:WORD_1
	v_fma_mixlo_f16 v4, v4, s8, -v16 op_sel_hi:[0,0,1]
	v_cvt_pk_f16_f32 v16, v0, v19
	v_cvt_pk_f16_f32 v19, v14, v15
	v_cvt_f32_f16_e32 v14, v19
	v_cvt_f32_f16_sdwa v15, v19 dst_sel:DWORD dst_unused:UNUSED_PAD src0_sel:WORD_1
	v_fma_mixlo_f16 v20, v5, s8, 0
	v_pk_fma_f32 v[6:7], v[6:7], s[8:9], v[12:13] op_sel_hi:[1,0,1] neg_lo:[0,0,1] neg_hi:[0,0,1]
	v_fma_mixhi_f16 v4, v5, s8, -v20 op_sel_hi:[0,0,1]
	v_cvt_pk_f16_f32 v5, v6, v7
	v_lshl_add_u64 v[6:7], s[6:7], 0, v[2:3]
	v_lshlrev_b32_e32 v0, 1, v54
	v_lshl_add_u64 v[2:3], s[2:3], 0, v[2:3]
	v_fma_mixlo_f16 v22, v9, s8, 0
	v_pk_fma_f32 v[10:11], v[10:11], s[8:9], v[14:15] op_sel_hi:[1,0,1] neg_lo:[0,0,1] neg_hi:[0,0,1]
	v_lshl_add_u64 v[6:7], v[6:7], 0, v[0:1]
	v_lshl_add_u64 v[0:1], v[2:3], 0, v[0:1]
	v_fma_mixhi_f16 v8, v9, s8, -v22 op_sel_hi:[0,0,1]
	v_cvt_pk_f16_f32 v9, v10, v11
	global_store_dwordx2 v[6:7], v[16:17], off
	global_store_dwordx2 v[6:7], v[18:19], off offset:512
	global_store_dwordx2 v[0:1], v[4:5], off
	global_store_dwordx2 v[0:1], v[8:9], off offset:512
	s_endpgm
	s_endpgm
	s_endpgm
	s_endpgm
	s_endpgm
	s_endpgm
	s_endpgm
	s_endpgm
	s_endpgm
	s_endpgm
	s_endpgm
	s_endpgm
	s_endpgm
	s_endpgm
	s_endpgm
	s_endpgm
	s_endpgm
	s_endpgm
	s_endpgm
	s_endpgm
	s_endpgm
	s_endpgm
	s_endpgm
	s_endpgm
	s_endpgm
	s_endpgm
	s_endpgm
	s_endpgm
	s_endpgm
	s_endpgm
	s_endpgm
	s_endpgm
	s_endpgm
	s_endpgm
	s_endpgm
	s_endpgm
	s_endpgm
	s_endpgm
	s_endpgm
	s_endpgm
	s_endpgm
	s_endpgm
	s_endpgm
	s_endpgm
	s_endpgm
	s_endpgm
	s_endpgm
	s_endpgm
	s_endpgm
	s_endpgm
	s_endpgm
	s_endpgm
	s_endpgm
	s_endpgm

.LBB21_5:
	v_lshlrev_b32_e32 v0, 2, v0
	v_and_b32_e32 v58, 0xfc, v0
	v_lshlrev_b64 v[4:5], 11, v[4:5]
	v_lshlrev_b32_e32 v0, 2, v58
	v_mov_b32_e32 v1, 0
	s_waitcnt lgkmcnt(0)
	v_lshl_add_u64 v[4:5], s[18:19], 0, v[4:5]
	v_lshl_add_u64 v[20:21], v[4:5], 0, v[0:1]
	global_load_dwordx4 v[4:7], v[20:21], off
	global_load_dwordx4 v[8:11], v0, s[16:17]
	global_load_dwordx4 v[12:15], v0, s[16:17] offset:1024
	global_load_dwordx4 v[16:19], v[20:21], off offset:1024
	s_load_dwordx2 s[0:1], s[0:1], 0x8
	v_lshlrev_b64 v[52:53], 11, v[2:3]
	v_lshl_add_u64 v[28:29], s[14:15], 0, v[52:53]
	v_lshl_add_u64 v[24:25], v[28:29], 0, v[0:1]
	v_mov_b32_e32 v59, 0x3727c5ac
	s_waitcnt lgkmcnt(0)
	v_lshl_add_u64 v[20:21], s[0:1], 2, v[28:29]
	v_lshl_add_u64 v[26:27], s[0:1], 3, v[28:29]
	v_lshl_add_u64 v[36:37], v[20:21], 0, v[0:1]
	global_load_dwordx4 v[20:23], v[24:25], off
	v_lshl_add_u64 v[40:41], v[26:27], 0, v[0:1]
	global_load_dwordx4 v[24:27], v[24:25], off offset:1024
	v_mad_u64_u32 v[44:45], s[12:13], s0, 12, v[28:29]
	v_mov_b32_e32 v38, v45
	v_mad_u64_u32 v[42:43], s[0:1], s1, 12, v[38:39]
	global_load_dwordx4 v[28:31], v[36:37], off
	global_load_dwordx4 v[32:35], v[36:37], off offset:1024
	v_mov_b32_e32 v45, v42
	global_load_dwordx4 v[36:39], v[40:41], off
	v_lshl_add_u64 v[54:55], v[44:45], 0, v[0:1]
	global_load_dwordx4 v[40:43], v[40:41], off offset:1024
	s_nop 0
	global_load_dwordx4 v[44:47], v[54:55], off
	global_load_dwordx4 v[48:51], v[54:55], off offset:1024
	v_mov_b32_e32 v60, 0x260
	v_lshlrev_b64 v[2:3], 10, v[2:3]
	s_waitcnt vmcnt(10)
	v_pk_add_f32 v[54:55], v[8:9], v[4:5]
	v_pk_add_f32 v[56:57], v[10:11], v[6:7]
	global_load_dwordx4 v[4:7], v0, s[8:9]
	global_load_dwordx4 v[8:11], v0, s[8:9] offset:1024
	s_waitcnt vmcnt(10)
	v_pk_add_f32 v[16:17], v[12:13], v[16:17]
	v_lshl_add_u64 v[12:13], s[4:5], 0, v[52:53]
	v_pk_add_f32 v[18:19], v[14:15], v[18:19]
	v_lshl_add_u64 v[52:53], v[12:13], 0, v[0:1]
	global_load_dwordx4 v[12:15], v0, s[10:11]
	s_mov_b32 s9, 0xf800000
	s_mov_b32 s8, 0x43000000
	s_waitcnt vmcnt(10)
	v_pk_add_f32 v[20:21], v[54:55], v[20:21]
	v_pk_add_f32 v[22:23], v[56:57], v[22:23]
	s_waitcnt vmcnt(9)
	v_pk_add_f32 v[24:25], v[16:17], v[24:25]
	v_pk_add_f32 v[26:27], v[18:19], v[26:27]
	global_load_dwordx4 v[16:19], v0, s[10:11] offset:1024
	s_waitcnt vmcnt(9)
	v_pk_add_f32 v[20:21], v[20:21], v[28:29]
	v_pk_add_f32 v[22:23], v[22:23], v[30:31]
	s_waitcnt vmcnt(8)
	v_pk_add_f32 v[24:25], v[24:25], v[32:33]
	s_waitcnt vmcnt(7)
	v_pk_add_f32 v[20:21], v[20:21], v[36:37]
	v_pk_add_f32 v[22:23], v[22:23], v[38:39]
	s_waitcnt vmcnt(5)
	v_pk_add_f32 v[20:21], v[20:21], v[44:45]
	v_pk_add_f32 v[22:23], v[22:23], v[46:47]
	v_add_f32_e32 v0, 0, v20
	v_add_f32_e32 v0, v0, v21
	v_pk_add_f32 v[24:25], v[24:25], v[40:41]
	v_add_f32_e32 v0, v0, v22
	v_pk_add_f32 v[26:27], v[26:27], v[34:35]
	s_waitcnt vmcnt(4)
	v_pk_add_f32 v[24:25], v[24:25], v[48:49]
	v_add_f32_e32 v0, v0, v23
	v_pk_add_f32 v[26:27], v[26:27], v[42:43]
	v_add_f32_e32 v0, v0, v24
	v_pk_add_f32 v[26:27], v[26:27], v[50:51]
	v_add_f32_e32 v0, v0, v25
	v_add_f32_e32 v0, v0, v26
	v_add_f32_e32 v0, v0, v27
	s_nop 1
	v_add_f32_dpp v0, v0, v0 quad_perm:[1,0,3,2] row_mask:0xf bank_mask:0xf bound_ctrl:1
	s_nop 1
	v_add_f32_dpp v0, v0, v0 quad_perm:[2,3,0,1] row_mask:0xf bank_mask:0xf bound_ctrl:1
	s_nop 1
	v_add_f32_dpp v0, v0, v0 row_half_mirror row_mask:0xf bank_mask:0xf bound_ctrl:1
	s_nop 1
	v_add_f32_dpp v0, v0, v0 row_mirror row_mask:0xf bank_mask:0xf bound_ctrl:1
	s_nop 0
	v_readlane_b32 s4, v0, 16
	v_readlane_b32 s5, v0, 48
	v_readlane_b32 s0, v0, 0
	v_readlane_b32 s1, v0, 32
	v_mov_b32_e32 v28, s4
	v_mov_b32_e32 v29, s5
	v_pk_add_f32 v[28:29], s[0:1], v[28:29]
	s_nop 0
	v_add_f32_e32 v0, v28, v29
	v_mul_f32_e32 v0, 0x3b000000, v0
	v_pk_add_f32 v[20:21], v[20:21], v[0:1] op_sel_hi:[1,0] neg_lo:[0,1] neg_hi:[0,1]
	v_pk_add_f32 v[22:23], v[22:23], v[0:1] op_sel_hi:[1,0] neg_lo:[0,1] neg_hi:[0,1]
	v_pk_mul_f32 v[28:29], v[20:21], v[20:21]
	v_pk_add_f32 v[24:25], v[24:25], v[0:1] op_sel_hi:[1,0] neg_lo:[0,1] neg_hi:[0,1]
	v_pk_add_f32 v[26:27], v[26:27], v[0:1] op_sel_hi:[1,0] neg_lo:[0,1] neg_hi:[0,1]
	v_pk_mul_f32 v[30:31], v[22:23], v[22:23]
	v_add_f32_e32 v0, v28, v29
	v_add_f32_e32 v0, v0, v30
	v_pk_mul_f32 v[32:33], v[24:25], v[24:25]
	v_add_f32_e32 v0, v0, v31
	v_add_f32_e32 v0, v0, v32
	v_pk_mul_f32 v[34:35], v[26:27], v[26:27]
	v_add_f32_e32 v0, v0, v33
	v_add_f32_e32 v0, v0, v34
	v_add_f32_e32 v0, v0, v35
	s_waitcnt vmcnt(3)
	v_pk_mul_f32 v[4:5], v[4:5], v[20:21]
	v_add_f32_dpp v0, v0, v0 quad_perm:[1,0,3,2] row_mask:0xf bank_mask:0xf bound_ctrl:1
	v_pk_mul_f32 v[6:7], v[6:7], v[22:23]
	s_waitcnt vmcnt(2)
	v_pk_mul_f32 v[8:9], v[8:9], v[24:25]
	v_add_f32_dpp v0, v0, v0 quad_perm:[2,3,0,1] row_mask:0xf bank_mask:0xf bound_ctrl:1
	v_pk_mul_f32 v[10:11], v[10:11], v[26:27]
	s_nop 0
	v_add_f32_dpp v0, v0, v0 row_half_mirror row_mask:0xf bank_mask:0xf bound_ctrl:1
	s_nop 1
	v_add_f32_dpp v0, v0, v0 row_mirror row_mask:0xf bank_mask:0xf bound_ctrl:1
	s_nop 0
	v_readlane_b32 s4, v0, 16
	v_readlane_b32 s5, v0, 48
	v_readlane_b32 s0, v0, 0
	v_readlane_b32 s1, v0, 32
	v_mov_b32_e32 v28, s4
	v_mov_b32_e32 v29, s5
	v_pk_add_f32 v[28:29], s[0:1], v[28:29]
	s_nop 0
	v_add_f32_e32 v0, v28, v29
	v_fmac_f32_e32 v59, 0x3b000000, v0
	v_mul_f32_e32 v0, 0x4f800000, v59
	v_cmp_gt_f32_e32 vcc, s9, v59
	s_nop 1
	v_cndmask_b32_e32 v0, v59, v0, vcc
	v_sqrt_f32_e32 v28, v0
	s_nop 0
	v_add_u32_e32 v20, -1, v28
	v_add_u32_e32 v21, 1, v28
	v_fma_f32 v22, -v20, v28, v0
	v_fma_f32 v23, -v21, v28, v0
	v_cmp_ge_f32_e64 s[0:1], 0, v22
	s_nop 1
	v_cndmask_b32_e64 v20, v28, v20, s[0:1]
	v_cmp_lt_f32_e64 s[0:1], 0, v23
	s_nop 1
	v_cndmask_b32_e64 v20, v20, v21, s[0:1]
	v_mul_f32_e32 v21, 0x37800000, v20
	v_cndmask_b32_e32 v20, v20, v21, vcc
	v_cmp_class_f32_e32 vcc, v0, v60
	s_nop 1
	v_cndmask_b32_e32 v0, v20, v0, vcc
	v_div_scale_f32 v20, s[0:1], v0, v0, 1.0
	v_rcp_f32_e32 v21, v20
	v_div_scale_f32 v22, vcc, 1.0, v0, 1.0
	v_fma_f32 v23, -v20, v21, 1.0
	v_fmac_f32_e32 v21, v23, v21
	v_mul_f32_e32 v23, v22, v21
	v_fma_f32 v24, -v20, v23, v22
	v_fmac_f32_e32 v23, v24, v21
	v_fma_f32 v20, -v20, v23, v22
	v_div_fmas_f32 v20, v20, v21, v23
	v_div_fixup_f32 v0, v20, v0, 1.0
	s_waitcnt vmcnt(1)
	v_pk_fma_f32 v[4:5], v[0:1], v[4:5], v[12:13] op_sel_hi:[0,1,1]
	v_pk_fma_f32 v[6:7], v[0:1], v[6:7], v[14:15] op_sel_hi:[0,1,1]
	s_waitcnt vmcnt(0)
	v_pk_fma_f32 v[8:9], v[0:1], v[8:9], v[16:17] op_sel_hi:[0,1,1]
	v_fma_mixlo_f16 v12, v4, s8, 0
	v_pk_fma_f32 v[10:11], v[0:1], v[10:11], v[18:19] op_sel_hi:[0,1,1]
	global_store_dwordx4 v[52:53], v[4:7], off
	global_store_dwordx4 v[52:53], v[8:11], off offset:1024
	v_mul_f32_e32 v0, 0x43000000, v4
	v_fma_mixlo_f16 v4, v4, s8, -v12 op_sel_hi:[0,0,1]
	v_fma_mixlo_f16 v12, v8, s8, 0
	v_mul_f32_e32 v13, 0x43000000, v8
	v_fma_mixlo_f16 v8, v8, s8, -v12 op_sel_hi:[0,0,1]
	v_mul_f32_e32 v12, 0x43000000, v5
	v_fma_mixlo_f16 v14, v5, s8, 0
	v_cvt_pk_f16_f32 v12, v0, v12
	v_mul_f32_e32 v0, 0x43000000, v9
	v_pk_mul_f32 v[16:17], v[6:7], s[8:9] op_sel_hi:[1,0]
	v_fma_mixhi_f16 v4, v5, s8, -v14 op_sel_hi:[0,0,1]
	v_cvt_pk_f16_f32 v14, v13, v0
	v_cvt_pk_f16_f32 v13, v16, v17
	v_pk_mul_f32 v[18:19], v[10:11], s[8:9] op_sel_hi:[1,0]
	v_cvt_f32_f16_e32 v16, v13
	v_cvt_f32_f16_sdwa v17, v13 dst_sel:DWORD dst_unused:UNUSED_PAD src0_sel:WORD_1
	v_cvt_pk_f16_f32 v15, v18, v19
	v_cvt_f32_f16_e32 v18, v15
	v_cvt_f32_f16_sdwa v19, v15 dst_sel:DWORD dst_unused:UNUSED_PAD src0_sel:WORD_1
	v_fma_mixlo_f16 v5, v9, s8, 0
	v_pk_fma_f32 v[6:7], v[6:7], s[8:9], v[16:17] op_sel_hi:[1,0,1] neg_lo:[0,0,1] neg_hi:[0,0,1]
	v_fma_mixhi_f16 v8, v9, s8, -v5 op_sel_hi:[0,0,1]
	v_cvt_pk_f16_f32 v5, v6, v7
	v_pk_fma_f32 v[6:7], v[10:11], s[8:9], v[18:19] op_sel_hi:[1,0,1] neg_lo:[0,0,1] neg_hi:[0,0,1]
	v_lshlrev_b32_e32 v0, 1, v58
	v_cvt_pk_f16_f32 v9, v6, v7
	v_lshl_add_u64 v[6:7], s[6:7], 0, v[2:3]
	v_lshl_add_u64 v[2:3], s[2:3], 0, v[2:3]
	v_lshl_add_u64 v[6:7], v[6:7], 0, v[0:1]
	v_lshl_add_u64 v[0:1], v[2:3], 0, v[0:1]
	global_store_dwordx2 v[6:7], v[12:13], off
	global_store_dwordx2 v[6:7], v[14:15], off offset:512
	global_store_dwordx2 v[0:1], v[4:5], off
	global_store_dwordx2 v[0:1], v[8:9], off offset:512
	s_endpgm
	s_endpgm
	s_endpgm
	s_endpgm
	s_endpgm
	s_endpgm
	s_endpgm
	s_endpgm
	s_endpgm
	s_endpgm
	s_endpgm
	s_endpgm
	s_endpgm

.LBB22_5:
	v_lshlrev_b32_e32 v0, 2, v0
	v_and_b32_e32 v66, 0xfc, v0
	v_lshlrev_b64 v[4:5], 11, v[4:5]
	v_lshlrev_b32_e32 v0, 2, v66
	v_mov_b32_e32 v1, 0
	s_waitcnt lgkmcnt(0)
	v_lshl_add_u64 v[4:5], s[18:19], 0, v[4:5]
	v_lshl_add_u64 v[20:21], v[4:5], 0, v[0:1]
	global_load_dwordx4 v[4:7], v[20:21], off
	global_load_dwordx4 v[8:11], v0, s[16:17]
	global_load_dwordx4 v[12:15], v0, s[16:17] offset:1024
	global_load_dwordx4 v[16:19], v[20:21], off offset:1024
	v_lshlrev_b64 v[48:49], 11, v[2:3]
	v_lshl_add_u64 v[40:41], s[14:15], 0, v[48:49]
	v_lshl_add_u64 v[28:29], v[40:41], 0, v[0:1]
	global_load_dwordx4 v[20:23], v[28:29], off
	global_load_dwordx4 v[24:27], v[28:29], off offset:1024
	s_load_dwordx2 s[0:1], s[0:1], 0x8
	v_lshlrev_b64 v[2:3], 10, v[2:3]
	s_waitcnt lgkmcnt(0)
	v_lshl_add_u64 v[28:29], s[0:1], 2, v[40:41]
	v_lshl_add_u64 v[42:43], v[28:29], 0, v[0:1]
	v_mad_u64_u32 v[36:37], s[12:13], s0, 12, v[40:41]
	v_lshl_add_u64 v[32:33], s[0:1], 3, v[40:41]
	global_load_dwordx4 v[28:31], v[42:43], off
	v_mov_b32_e32 v38, v37
	v_lshl_add_u64 v[44:45], v[32:33], 0, v[0:1]
	v_mad_u64_u32 v[38:39], s[12:13], s1, 12, v[38:39]
	global_load_dwordx4 v[32:35], v[44:45], off
	v_mov_b32_e32 v37, v38
	v_lshl_add_u64 v[46:47], v[36:37], 0, v[0:1]
	global_load_dwordx4 v[36:39], v[46:47], off
	v_mad_u64_u32 v[52:53], s[12:13], s0, 20, v[40:41]
	v_mad_u64_u32 v[54:55], s[12:13], s0, 24, v[40:41]
	v_lshl_add_u64 v[50:51], s[0:1], 4, v[40:41]
	v_mad_u64_u32 v[40:41], s[12:13], s0, 28, v[40:41]
	v_lshl_add_u64 v[50:51], v[50:51], 0, v[0:1]
	s_waitcnt vmcnt(7)
	v_pk_add_f32 v[56:57], v[8:9], v[4:5]
	v_mov_b32_e32 v4, v53
	v_pk_add_f32 v[58:59], v[10:11], v[6:7]
	v_mov_b32_e32 v6, v55
	v_mad_u64_u32 v[10:11], s[12:13], s1, 20, v[4:5]
	s_waitcnt vmcnt(5)
	v_pk_add_f32 v[60:61], v[12:13], v[16:17]
	v_mov_b32_e32 v8, v41
	v_mad_u64_u32 v[12:13], s[12:13], s1, 24, v[6:7]
	v_mov_b32_e32 v53, v10
	v_pk_add_f32 v[62:63], v[14:15], v[18:19]
	v_mad_u64_u32 v[14:15], s[0:1], s1, 28, v[8:9]
	global_load_dwordx4 v[4:7], v[50:51], off
	v_mov_b32_e32 v55, v12
	v_lshl_add_u64 v[52:53], v[52:53], 0, v[0:1]
	v_mov_b32_e32 v41, v14
	v_lshl_add_u64 v[54:55], v[54:55], 0, v[0:1]
	global_load_dwordx4 v[12:15], v[52:53], off
	v_lshl_add_u64 v[64:65], v[40:41], 0, v[0:1]
	global_load_dwordx4 v[16:19], v[54:55], off
	global_load_dwordx4 v[8:11], v[42:43], off offset:1024
	s_waitcnt vmcnt(8)
	v_pk_add_f32 v[40:41], v[56:57], v[20:21]
	v_pk_add_f32 v[42:43], v[58:59], v[22:23]
	global_load_dwordx4 v[20:23], v[64:65], off
	s_waitcnt vmcnt(8)
	v_pk_add_f32 v[56:57], v[60:61], v[24:25]
	v_pk_add_f32 v[58:59], v[62:63], v[26:27]
	s_waitcnt vmcnt(7)
	v_pk_add_f32 v[40:41], v[40:41], v[28:29]
	v_pk_add_f32 v[42:43], v[42:43], v[30:31]
	global_load_dwordx4 v[24:27], v[44:45], off offset:1024
	global_load_dwordx4 v[28:31], v[46:47], off offset:1024
	s_waitcnt vmcnt(8)
	v_pk_add_f32 v[44:45], v[40:41], v[32:33]
	v_pk_add_f32 v[46:47], v[42:43], v[34:35]
	global_load_dwordx4 v[32:35], v[50:51], off offset:1024
	global_load_dwordx4 v[40:43], v[52:53], off offset:1024
	s_waitcnt vmcnt(9)
	v_pk_add_f32 v[50:51], v[44:45], v[36:37]
	v_pk_add_f32 v[52:53], v[46:47], v[38:39]
	global_load_dwordx4 v[36:39], v[54:55], off offset:1024
	global_load_dwordx4 v[44:47], v[64:65], off offset:1024
	s_waitcnt vmcnt(10)
	v_pk_add_f32 v[4:5], v[50:51], v[4:5]
	v_pk_add_f32 v[6:7], v[52:53], v[6:7]
	s_waitcnt vmcnt(9)
	v_pk_add_f32 v[50:51], v[4:5], v[12:13]
	v_pk_add_f32 v[52:53], v[6:7], v[14:15]
	global_load_dwordx4 v[4:7], v0, s[8:9]
	global_load_dwordx4 v[12:15], v0, s[10:11]
	s_waitcnt vmcnt(10)
	v_pk_add_f32 v[16:17], v[50:51], v[16:17]
	v_pk_add_f32 v[18:19], v[52:53], v[18:19]
	s_waitcnt vmcnt(9)
	v_pk_add_f32 v[8:9], v[56:57], v[8:9]
	s_waitcnt vmcnt(8)
	v_pk_add_f32 v[50:51], v[16:17], v[20:21]
	v_pk_add_f32 v[52:53], v[18:19], v[22:23]
	global_load_dwordx4 v[16:19], v0, s[8:9] offset:1024
	global_load_dwordx4 v[20:23], v0, s[10:11] offset:1024
	v_pk_add_f32 v[10:11], v[58:59], v[10:11]
	s_waitcnt vmcnt(9)
	v_pk_add_f32 v[8:9], v[8:9], v[24:25]
	v_add_f32_e32 v24, 0, v50
	s_waitcnt vmcnt(8)
	v_pk_add_f32 v[8:9], v[8:9], v[28:29]
	v_pk_add_f32 v[10:11], v[10:11], v[26:27]
	s_waitcnt vmcnt(7)
	v_pk_add_f32 v[8:9], v[8:9], v[32:33]
	v_add_f32_e32 v24, v24, v51
	s_waitcnt vmcnt(6)
	v_pk_add_f32 v[8:9], v[8:9], v[40:41]
	v_pk_add_f32 v[10:11], v[10:11], v[30:31]
	v_add_f32_e32 v24, v24, v52
	s_waitcnt vmcnt(5)
	v_pk_add_f32 v[8:9], v[8:9], v[36:37]
	v_pk_add_f32 v[10:11], v[10:11], v[34:35]
	v_add_f32_e32 v24, v24, v53
	s_waitcnt vmcnt(4)
	v_pk_add_f32 v[8:9], v[8:9], v[44:45]
	v_pk_add_f32 v[10:11], v[10:11], v[42:43]
	v_add_f32_e32 v24, v24, v8
	v_pk_add_f32 v[10:11], v[10:11], v[38:39]
	v_add_f32_e32 v24, v24, v9
	v_pk_add_f32 v[10:11], v[10:11], v[46:47]
	s_nop 0
	v_add_f32_e32 v24, v24, v10
	v_add_f32_e32 v24, v24, v11
	s_nop 1
	v_add_f32_dpp v24, v24, v24 quad_perm:[1,0,3,2] row_mask:0xf bank_mask:0xf bound_ctrl:1
	s_nop 1
	v_add_f32_dpp v24, v24, v24 quad_perm:[2,3,0,1] row_mask:0xf bank_mask:0xf bound_ctrl:1
	s_nop 1
	v_add_f32_dpp v24, v24, v24 row_half_mirror row_mask:0xf bank_mask:0xf bound_ctrl:1
	s_nop 1
	v_add_f32_dpp v24, v24, v24 row_mirror row_mask:0xf bank_mask:0xf bound_ctrl:1
	s_nop 0
	v_readlane_b32 s8, v24, 16
	v_readlane_b32 s9, v24, 48
	v_readlane_b32 s0, v24, 0
	v_readlane_b32 s1, v24, 32
	v_mov_b32_e32 v24, s8
	v_mov_b32_e32 v25, s9
	v_pk_add_f32 v[24:25], s[0:1], v[24:25]
	s_nop 0
	v_add_f32_e32 v24, v24, v25
	v_mul_f32_e32 v24, 0x3b000000, v24
	v_pk_add_f32 v[26:27], v[50:51], v[24:25] op_sel_hi:[1,0] neg_lo:[0,1] neg_hi:[0,1]
	v_pk_add_f32 v[30:31], v[52:53], v[24:25] op_sel_hi:[1,0] neg_lo:[0,1] neg_hi:[0,1]
	v_pk_mul_f32 v[28:29], v[26:27], v[26:27]
	v_pk_mul_f32 v[32:33], v[30:31], v[30:31]
	v_add_f32_e32 v28, v28, v29
	v_pk_add_f32 v[8:9], v[8:9], v[24:25] op_sel_hi:[1,0] neg_lo:[0,1] neg_hi:[0,1]
	v_add_f32_e32 v28, v28, v32
	v_pk_mul_f32 v[34:35], v[8:9], v[8:9]
	v_add_f32_e32 v28, v28, v33
	v_pk_add_f32 v[10:11], v[10:11], v[24:25] op_sel_hi:[1,0] neg_lo:[0,1] neg_hi:[0,1]
	v_add_f32_e32 v28, v28, v34
	v_pk_mul_f32 v[24:25], v[10:11], v[10:11]
	v_add_f32_e32 v28, v28, v35
	v_add_f32_e32 v24, v28, v24
	v_add_f32_e32 v24, v24, v25
	s_waitcnt vmcnt(3)
	v_pk_mul_f32 v[4:5], v[4:5], v[26:27]
	v_add_f32_dpp v24, v24, v24 quad_perm:[1,0,3,2] row_mask:0xf bank_mask:0xf bound_ctrl:1
	v_pk_mul_f32 v[6:7], v[6:7], v[30:31]
	s_waitcnt vmcnt(1)
	v_pk_mul_f32 v[8:9], v[16:17], v[8:9]
	v_add_f32_dpp v24, v24, v24 quad_perm:[2,3,0,1] row_mask:0xf bank_mask:0xf bound_ctrl:1
	v_pk_mul_f32 v[10:11], v[18:19], v[10:11]
	s_nop 0
	v_add_f32_dpp v24, v24, v24 row_half_mirror row_mask:0xf bank_mask:0xf bound_ctrl:1
	s_nop 1
	v_add_f32_dpp v24, v24, v24 row_mirror row_mask:0xf bank_mask:0xf bound_ctrl:1
	s_nop 0
	v_readlane_b32 s8, v24, 16
	v_readlane_b32 s9, v24, 48
	v_readlane_b32 s0, v24, 0
	v_readlane_b32 s1, v24, 32
	v_mov_b32_e32 v24, s8
	v_mov_b32_e32 v25, s9
	v_pk_add_f32 v[24:25], s[0:1], v[24:25]
	s_mov_b32 s0, 0xf800000
	v_add_f32_e32 v24, v24, v25
	v_mov_b32_e32 v25, 0x3727c5ac
	v_fmac_f32_e32 v25, 0x3b000000, v24
	v_mul_f32_e32 v24, 0x4f800000, v25
	v_cmp_gt_f32_e32 vcc, s0, v25
	s_nop 1
	v_cndmask_b32_e32 v24, v25, v24, vcc
	v_sqrt_f32_e32 v25, v24
	s_nop 0
	v_add_u32_e32 v28, -1, v25
	v_fma_f32 v29, -v28, v25, v24
	v_cmp_ge_f32_e64 s[0:1], 0, v29
	v_add_u32_e32 v29, 1, v25
	s_nop 0
	v_cndmask_b32_e64 v28, v25, v28, s[0:1]
	v_fma_f32 v25, -v29, v25, v24
	v_cmp_lt_f32_e64 s[0:1], 0, v25
	s_nop 1
	v_cndmask_b32_e64 v25, v28, v29, s[0:1]
	v_mul_f32_e32 v28, 0x37800000, v25
	v_cndmask_b32_e32 v25, v25, v28, vcc
	v_mov_b32_e32 v28, 0x260
	v_cmp_class_f32_e32 vcc, v24, v28
	s_nop 1
	v_cndmask_b32_e32 v28, v25, v24, vcc
	v_div_scale_f32 v29, s[0:1], v28, v28, 1.0
	v_rcp_f32_e32 v32, v29
	v_lshl_add_u64 v[24:25], s[4:5], 0, v[48:49]
	v_lshl_add_u64 v[24:25], v[24:25], 0, v[0:1]
	s_mov_b32 s0, 0x43000000
	v_fma_f32 v0, -v29, v32, 1.0
	v_fmac_f32_e32 v32, v0, v32
	v_div_scale_f32 v0, vcc, 1.0, v28, 1.0
	v_mul_f32_e32 v33, v0, v32
	v_fma_f32 v34, -v29, v33, v0
	v_fmac_f32_e32 v33, v34, v32
	v_fma_f32 v0, -v29, v33, v0
	v_div_fmas_f32 v0, v0, v32, v33
	v_div_fixup_f32 v0, v0, v28, 1.0
	v_pk_fma_f32 v[4:5], v[0:1], v[4:5], v[12:13] op_sel_hi:[0,1,1]
	v_pk_fma_f32 v[6:7], v[0:1], v[6:7], v[14:15] op_sel_hi:[0,1,1]
	s_waitcnt vmcnt(0)
	v_pk_fma_f32 v[8:9], v[0:1], v[8:9], v[20:21] op_sel_hi:[0,1,1]
	v_fma_mixlo_f16 v12, v4, s0, 0
	v_pk_fma_f32 v[10:11], v[0:1], v[10:11], v[22:23] op_sel_hi:[0,1,1]
	global_store_dwordx4 v[24:25], v[4:7], off
	global_store_dwordx4 v[24:25], v[8:11], off offset:1024
	v_mul_f32_e32 v0, 0x43000000, v4
	v_fma_mixlo_f16 v4, v4, s0, -v12 op_sel_hi:[0,0,1]
	v_fma_mixlo_f16 v12, v8, s0, 0
	v_mul_f32_e32 v13, 0x43000000, v8
	v_fma_mixlo_f16 v8, v8, s0, -v12 op_sel_hi:[0,0,1]
	v_mul_f32_e32 v12, 0x43000000, v5
	v_fma_mixlo_f16 v14, v5, s0, 0
	v_cvt_pk_f16_f32 v12, v0, v12
	v_mul_f32_e32 v0, 0x43000000, v9
	v_pk_mul_f32 v[16:17], v[6:7], s[0:1] op_sel_hi:[1,0]
	v_fma_mixhi_f16 v4, v5, s0, -v14 op_sel_hi:[0,0,1]
	v_cvt_pk_f16_f32 v14, v13, v0
	v_cvt_pk_f16_f32 v13, v16, v17
	v_pk_mul_f32 v[18:19], v[10:11], s[0:1] op_sel_hi:[1,0]
	v_cvt_f32_f16_e32 v16, v13
	v_cvt_f32_f16_sdwa v17, v13 dst_sel:DWORD dst_unused:UNUSED_PAD src0_sel:WORD_1
	v_cvt_pk_f16_f32 v15, v18, v19
	v_cvt_f32_f16_e32 v18, v15
	v_cvt_f32_f16_sdwa v19, v15 dst_sel:DWORD dst_unused:UNUSED_PAD src0_sel:WORD_1
	v_fma_mixlo_f16 v5, v9, s0, 0
	v_pk_fma_f32 v[6:7], v[6:7], s[0:1], v[16:17] op_sel_hi:[1,0,1] neg_lo:[0,0,1] neg_hi:[0,0,1]
	v_fma_mixhi_f16 v8, v9, s0, -v5 op_sel_hi:[0,0,1]
	v_cvt_pk_f16_f32 v5, v6, v7
	v_pk_fma_f32 v[6:7], v[10:11], s[0:1], v[18:19] op_sel_hi:[1,0,1] neg_lo:[0,0,1] neg_hi:[0,0,1]
	v_lshlrev_b32_e32 v0, 1, v66
	v_cvt_pk_f16_f32 v9, v6, v7
	v_lshl_add_u64 v[6:7], s[6:7], 0, v[2:3]
	v_lshl_add_u64 v[2:3], s[2:3], 0, v[2:3]
	v_lshl_add_u64 v[6:7], v[6:7], 0, v[0:1]
	v_lshl_add_u64 v[0:1], v[2:3], 0, v[0:1]
	global_store_dwordx2 v[6:7], v[12:13], off
	global_store_dwordx2 v[6:7], v[14:15], off offset:512
	global_store_dwordx2 v[0:1], v[4:5], off
	global_store_dwordx2 v[0:1], v[8:9], off offset:512
	s_endpgm
	s_endpgm
	s_endpgm
	s_endpgm
	s_endpgm
	s_endpgm
	s_endpgm
	s_endpgm
	s_endpgm
	s_endpgm
	s_endpgm
	s_endpgm
	s_endpgm
	s_endpgm
	s_endpgm
	s_endpgm
	s_endpgm
	s_endpgm
	s_endpgm
	s_endpgm
	s_endpgm
	s_endpgm
	s_endpgm
	s_endpgm
	s_endpgm
	s_endpgm
	s_endpgm
	s_endpgm
	s_endpgm
	s_endpgm
	s_endpgm
	s_endpgm
	s_endpgm
	s_endpgm
	s_endpgm
	s_endpgm
	s_endpgm
	s_endpgm
	s_endpgm
	s_endpgm
	s_endpgm
	s_endpgm
	s_endpgm
	s_endpgm
	s_endpgm
	s_endpgm
	s_endpgm
	s_endpgm
	s_endpgm
	s_endpgm
	s_endpgm
	s_endpgm
	s_endpgm
	s_endpgm
	s_endpgm
	s_endpgm
	s_endpgm
	s_endpgm
